# SGU LayerNorm statistics batched (8 tokens per batch, 16 loads in flight, batched butterfly)
# baseline (speedup 1.0000x reference)
; __device__ __forceinline__ float wave_sum(float v) {
; #pragma unroll
;     for (int o = 1; o < 64; o <<= 1) v += __shfl_xor(v, o);
; __device__ __forceinline__ void unit(LAS unsigned char* lds, const bf16* Z, const bf16* sgw, const float* lng, const float* lnb, const float* sgb, bf16* OBp, int b, int nchunk, int g0, int ng, const int tid_in) {
;     ...
;     for (int k = 0; k < 16; ++k) { const int tok = 16 * w + k; const bf16* row = Z + (size_t)(tb0 + tok) * ZLD + ZV;
;         float s = 0.f, ss = 0.f;
; #pragma unroll
;         for (int q = 0; q < 2; ++q) { const v4u vv = *(const v4u*)(row + q * 512 + lane * 8); const unsigned ww[4] = {vv.x, vv.y, vv.z, vv.w};
; #pragma unroll
;             for (int e = 0; e < 4; ++e) { const float a = bflo(ww[e]), c = bfhi(ww[e]); s += a + c; ss += a * a + c * c; } }
.LBB0_289:
	v_and_b32_e32 v2, 64, v228
	v_add_u32_e32 v2, 64, v2
	v_xor_b32_e32 v3, 1, v228
	v_cmp_lt_i32_e32 vcc, v3, v2
	v_mov_b32_e32 v70, v1
	s_and_b32 s4, s19, 0xffffff80
	v_cndmask_b32_e32 v3, v228, v3, vcc
	v_lshlrev_b32_e32 v5, 2, v3
	v_xor_b32_e32 v3, 2, v228
	v_cmp_lt_i32_e32 vcc, v3, v2
	v_readfirstlane_b32 s23, v70
	s_ashr_i32 s22, s23, 6
	v_cndmask_b32_e32 v3, v228, v3, vcc
	v_lshlrev_b32_e32 v6, 2, v3
	v_xor_b32_e32 v3, 4, v228
	v_cmp_lt_i32_e32 vcc, v3, v2
	s_lshl_b32 s5, s22, 4
	s_lshl_b32 s14, s22, 7
	v_cndmask_b32_e32 v3, v228, v3, vcc
	v_lshlrev_b32_e32 v7, 2, v3
	v_xor_b32_e32 v3, 8, v228
	v_cmp_lt_i32_e32 vcc, v3, v2
	s_add_i32 s4, s4, s5
	s_add_i32 s28, s14, 0
	v_cndmask_b32_e32 v3, v228, v3, vcc
	v_lshlrev_b32_e32 v8, 2, v3
	v_xor_b32_e32 v3, 16, v228
	v_cmp_lt_i32_e32 vcc, v3, v2
	s_mul_hi_i32 s5, s4, 0x4600
	s_mulk_i32 s4, 0x4600
	v_cndmask_b32_e32 v3, v228, v3, vcc
	v_lshlrev_b32_e32 v9, 2, v3
	v_xor_b32_e32 v3, 32, v228
	v_readlane_b32 s14, v254, 10
	v_and_b32_e32 v4, 63, v70
	v_cmp_lt_i32_e32 vcc, v3, v2
	s_add_u32 s4, s14, s4
	v_readlane_b32 s14, v254, 11
	v_cndmask_b32_e32 v2, v228, v3, vcc
	v_lshlrev_b32_e32 v186, 4, v4
	s_addc_u32 s5, s14, s5
	s_mov_b32 s21, 0
	v_lshlrev_b32_e32 v10, 2, v2
	v_cmp_eq_u32_e64 s[0:1], 0, v4
	v_lshl_add_u64 v[2:3], s[4:5], 0, v[186:187]
	s_mov_b64 s[4:5], 0x4600
	global_load_dwordx4 v[20:23], v[2:3], off
	global_load_dwordx4 v[24:27], v[2:3], off offset:1024
	v_lshl_add_u64 v[2:3], v[2:3], 0, s[4:5]
	global_load_dwordx4 v[28:31], v[2:3], off
	global_load_dwordx4 v[32:35], v[2:3], off offset:1024
	v_lshl_add_u64 v[2:3], v[2:3], 0, s[4:5]
	global_load_dwordx4 v[36:39], v[2:3], off
	global_load_dwordx4 v[40:43], v[2:3], off offset:1024
	v_lshl_add_u64 v[2:3], v[2:3], 0, s[4:5]
	global_load_dwordx4 v[44:47], v[2:3], off
	global_load_dwordx4 v[48:51], v[2:3], off offset:1024
	v_lshl_add_u64 v[2:3], v[2:3], 0, s[4:5]
	global_load_dwordx4 v[52:55], v[2:3], off
	global_load_dwordx4 v[56:59], v[2:3], off offset:1024
	v_lshl_add_u64 v[2:3], v[2:3], 0, s[4:5]
	global_load_dwordx4 v[60:63], v[2:3], off
	global_load_dwordx4 v[64:67], v[2:3], off offset:1024
	v_lshl_add_u64 v[2:3], v[2:3], 0, s[4:5]
	global_load_dwordx4 v[72:75], v[2:3], off
	global_load_dwordx4 v[76:79], v[2:3], off offset:1024
	v_lshl_add_u64 v[2:3], v[2:3], 0, s[4:5]
	global_load_dwordx4 v[80:83], v[2:3], off
	global_load_dwordx4 v[84:87], v[2:3], off offset:1024
	v_lshl_add_u64 v[2:3], v[2:3], 0, s[4:5]
	s_waitcnt vmcnt(14)
	v_lshlrev_b32_e32 v68, 16, v20
	v_and_b32_e32 v20, 0xffff0000, v20
	v_add_f32_e32 v69, v68, v20
	v_mul_f32_e32 v20, v20, v20
	v_fmac_f32_e32 v20, v68, v68
	v_add_f32_e32 v88, 0, v69
	v_lshlrev_b32_e32 v68, 16, v21
	v_and_b32_e32 v21, 0xffff0000, v21
	v_add_f32_e32 v69, v68, v21
	v_mul_f32_e32 v21, v21, v21
	v_fmac_f32_e32 v21, v68, v68
	v_add_f32_e32 v88, v69, v88
	v_add_f32_e32 v96, v20, v21
	v_lshlrev_b32_e32 v68, 16, v22
	v_and_b32_e32 v22, 0xffff0000, v22
	v_add_f32_e32 v69, v68, v22
	v_mul_f32_e32 v22, v22, v22
	v_fmac_f32_e32 v22, v68, v68
	v_add_f32_e32 v88, v69, v88
	v_add_f32_e32 v96, v22, v96
	v_lshlrev_b32_e32 v68, 16, v23
	v_and_b32_e32 v23, 0xffff0000, v23
	v_add_f32_e32 v69, v68, v23
	v_mul_f32_e32 v23, v23, v23
	v_fmac_f32_e32 v23, v68, v68
	v_add_f32_e32 v88, v69, v88
	v_add_f32_e32 v96, v23, v96
	v_lshlrev_b32_e32 v68, 16, v24
	v_and_b32_e32 v24, 0xffff0000, v24
	v_add_f32_e32 v69, v68, v24
	v_mul_f32_e32 v24, v24, v24
	v_fmac_f32_e32 v24, v68, v68
	v_add_f32_e32 v88, v69, v88
	v_add_f32_e32 v96, v24, v96
	v_lshlrev_b32_e32 v68, 16, v25
	v_and_b32_e32 v25, 0xffff0000, v25
	v_add_f32_e32 v69, v68, v25
	v_mul_f32_e32 v25, v25, v25
	v_fmac_f32_e32 v25, v68, v68
	v_add_f32_e32 v88, v69, v88
	v_add_f32_e32 v96, v25, v96
	v_lshlrev_b32_e32 v68, 16, v26
	v_and_b32_e32 v26, 0xffff0000, v26
	v_add_f32_e32 v69, v68, v26
	v_mul_f32_e32 v26, v26, v26
	v_fmac_f32_e32 v26, v68, v68
	v_add_f32_e32 v88, v69, v88
	v_add_f32_e32 v96, v26, v96
	v_lshlrev_b32_e32 v68, 16, v27
	v_and_b32_e32 v27, 0xffff0000, v27
	v_add_f32_e32 v69, v68, v27
	v_mul_f32_e32 v27, v27, v27
	v_fmac_f32_e32 v27, v68, v68
	v_add_f32_e32 v88, v69, v88
	v_add_f32_e32 v96, v27, v96
	s_waitcnt vmcnt(12)
	v_lshlrev_b32_e32 v68, 16, v28
	v_and_b32_e32 v28, 0xffff0000, v28
	v_add_f32_e32 v69, v68, v28
	v_mul_f32_e32 v28, v28, v28
	v_fmac_f32_e32 v28, v68, v68
	v_add_f32_e32 v89, 0, v69
	v_lshlrev_b32_e32 v68, 16, v29
	v_and_b32_e32 v29, 0xffff0000, v29
	v_add_f32_e32 v69, v68, v29
	v_mul_f32_e32 v29, v29, v29
	v_fmac_f32_e32 v29, v68, v68
	v_add_f32_e32 v89, v69, v89
	v_add_f32_e32 v97, v28, v29
	v_lshlrev_b32_e32 v68, 16, v30
	v_and_b32_e32 v30, 0xffff0000, v30
	v_add_f32_e32 v69, v68, v30
	v_mul_f32_e32 v30, v30, v30
	v_fmac_f32_e32 v30, v68, v68
	v_add_f32_e32 v89, v69, v89
	v_add_f32_e32 v97, v30, v97
	v_lshlrev_b32_e32 v68, 16, v31
	v_and_b32_e32 v31, 0xffff0000, v31
	v_add_f32_e32 v69, v68, v31
	v_mul_f32_e32 v31, v31, v31
	v_fmac_f32_e32 v31, v68, v68
	v_add_f32_e32 v89, v69, v89
	v_add_f32_e32 v97, v31, v97
	v_lshlrev_b32_e32 v68, 16, v32
	v_and_b32_e32 v32, 0xffff0000, v32
	v_add_f32_e32 v69, v68, v32
	v_mul_f32_e32 v32, v32, v32
	v_fmac_f32_e32 v32, v68, v68
	v_add_f32_e32 v89, v69, v89
	v_add_f32_e32 v97, v32, v97
	v_lshlrev_b32_e32 v68, 16, v33
	v_and_b32_e32 v33, 0xffff0000, v33
	v_add_f32_e32 v69, v68, v33
	v_mul_f32_e32 v33, v33, v33
	v_fmac_f32_e32 v33, v68, v68
	v_add_f32_e32 v89, v69, v89
	v_add_f32_e32 v97, v33, v97
	v_lshlrev_b32_e32 v68, 16, v34
	v_and_b32_e32 v34, 0xffff0000, v34
	v_add_f32_e32 v69, v68, v34
	v_mul_f32_e32 v34, v34, v34
	v_fmac_f32_e32 v34, v68, v68
	v_add_f32_e32 v89, v69, v89
	v_add_f32_e32 v97, v34, v97
	v_lshlrev_b32_e32 v68, 16, v35
	v_and_b32_e32 v35, 0xffff0000, v35
	v_add_f32_e32 v69, v68, v35
	v_mul_f32_e32 v35, v35, v35
	v_fmac_f32_e32 v35, v68, v68
	v_add_f32_e32 v89, v69, v89
	v_add_f32_e32 v97, v35, v97
	s_waitcnt vmcnt(10)
; __device__ __forceinline__ void unit(LAS unsigned char* lds, const bf16* Z, const bf16* sgw, const float* lng, const float* lnb, const float* sgb, bf16* OBp, int b, int nchunk, int g0, int ng, const int tid_in) {
;     ...
;         for (int q = 0; q < 2; ++q) { const v4u vv = *(const v4u*)(row + q * 512 + lane * 8); const unsigned ww[4] = {vv.x, vv.y, vv.z, vv.w};
; #pragma unroll
;             for (int e = 0; e < 4; ++e) { const float a = bflo(ww[e]), c = bfhi(ww[e]); s += a + c; ss += a * a + c * c; } }
	v_lshlrev_b32_e32 v68, 16, v36
	v_and_b32_e32 v36, 0xffff0000, v36
	v_add_f32_e32 v69, v68, v36
	v_mul_f32_e32 v36, v36, v36
	v_fmac_f32_e32 v36, v68, v68
	v_add_f32_e32 v90, 0, v69
	v_lshlrev_b32_e32 v68, 16, v37
	v_and_b32_e32 v37, 0xffff0000, v37
	v_add_f32_e32 v69, v68, v37
	v_mul_f32_e32 v37, v37, v37
	v_fmac_f32_e32 v37, v68, v68
	v_add_f32_e32 v90, v69, v90
	v_add_f32_e32 v98, v36, v37
	v_lshlrev_b32_e32 v68, 16, v38
	v_and_b32_e32 v38, 0xffff0000, v38
	v_add_f32_e32 v69, v68, v38
	v_mul_f32_e32 v38, v38, v38
	v_fmac_f32_e32 v38, v68, v68
	v_add_f32_e32 v90, v69, v90
	v_add_f32_e32 v98, v38, v98
	v_lshlrev_b32_e32 v68, 16, v39
	v_and_b32_e32 v39, 0xffff0000, v39
	v_add_f32_e32 v69, v68, v39
	v_mul_f32_e32 v39, v39, v39
	v_fmac_f32_e32 v39, v68, v68
	v_add_f32_e32 v90, v69, v90
	v_add_f32_e32 v98, v39, v98
	v_lshlrev_b32_e32 v68, 16, v40
	v_and_b32_e32 v40, 0xffff0000, v40
	v_add_f32_e32 v69, v68, v40
	v_mul_f32_e32 v40, v40, v40
	v_fmac_f32_e32 v40, v68, v68
	v_add_f32_e32 v90, v69, v90
	v_add_f32_e32 v98, v40, v98
	v_lshlrev_b32_e32 v68, 16, v41
	v_and_b32_e32 v41, 0xffff0000, v41
	v_add_f32_e32 v69, v68, v41
	v_mul_f32_e32 v41, v41, v41
	v_fmac_f32_e32 v41, v68, v68
	v_add_f32_e32 v90, v69, v90
	v_add_f32_e32 v98, v41, v98
	v_lshlrev_b32_e32 v68, 16, v42
	v_and_b32_e32 v42, 0xffff0000, v42
	v_add_f32_e32 v69, v68, v42
	v_mul_f32_e32 v42, v42, v42
	v_fmac_f32_e32 v42, v68, v68
	v_add_f32_e32 v90, v69, v90
	v_add_f32_e32 v98, v42, v98
	v_lshlrev_b32_e32 v68, 16, v43
	v_and_b32_e32 v43, 0xffff0000, v43
	v_add_f32_e32 v69, v68, v43
	v_mul_f32_e32 v43, v43, v43
	v_fmac_f32_e32 v43, v68, v68
	v_add_f32_e32 v90, v69, v90
	v_add_f32_e32 v98, v43, v98
	s_waitcnt vmcnt(8)
	v_lshlrev_b32_e32 v68, 16, v44
	v_and_b32_e32 v44, 0xffff0000, v44
	v_add_f32_e32 v69, v68, v44
	v_mul_f32_e32 v44, v44, v44
	v_fmac_f32_e32 v44, v68, v68
	v_add_f32_e32 v91, 0, v69
	v_lshlrev_b32_e32 v68, 16, v45
	v_and_b32_e32 v45, 0xffff0000, v45
	v_add_f32_e32 v69, v68, v45
	v_mul_f32_e32 v45, v45, v45
	v_fmac_f32_e32 v45, v68, v68
	v_add_f32_e32 v91, v69, v91
	v_add_f32_e32 v99, v44, v45
	v_lshlrev_b32_e32 v68, 16, v46
	v_and_b32_e32 v46, 0xffff0000, v46
	v_add_f32_e32 v69, v68, v46
	v_mul_f32_e32 v46, v46, v46
	v_fmac_f32_e32 v46, v68, v68
	v_add_f32_e32 v91, v69, v91
	v_add_f32_e32 v99, v46, v99
	v_lshlrev_b32_e32 v68, 16, v47
	v_and_b32_e32 v47, 0xffff0000, v47
	v_add_f32_e32 v69, v68, v47
	v_mul_f32_e32 v47, v47, v47
	v_fmac_f32_e32 v47, v68, v68
	v_add_f32_e32 v91, v69, v91
	v_add_f32_e32 v99, v47, v99
	v_lshlrev_b32_e32 v68, 16, v48
	v_and_b32_e32 v48, 0xffff0000, v48
	v_add_f32_e32 v69, v68, v48
	v_mul_f32_e32 v48, v48, v48
	v_fmac_f32_e32 v48, v68, v68
	v_add_f32_e32 v91, v69, v91
	v_add_f32_e32 v99, v48, v99
	v_lshlrev_b32_e32 v68, 16, v49
	v_and_b32_e32 v49, 0xffff0000, v49
	v_add_f32_e32 v69, v68, v49
	v_mul_f32_e32 v49, v49, v49
	v_fmac_f32_e32 v49, v68, v68
	v_add_f32_e32 v91, v69, v91
	v_add_f32_e32 v99, v49, v99
	v_lshlrev_b32_e32 v68, 16, v50
	v_and_b32_e32 v50, 0xffff0000, v50
	v_add_f32_e32 v69, v68, v50
	v_mul_f32_e32 v50, v50, v50
	v_fmac_f32_e32 v50, v68, v68
	v_add_f32_e32 v91, v69, v91
	v_add_f32_e32 v99, v50, v99
	v_lshlrev_b32_e32 v68, 16, v51
	v_and_b32_e32 v51, 0xffff0000, v51
	v_add_f32_e32 v69, v68, v51
	v_mul_f32_e32 v51, v51, v51
	v_fmac_f32_e32 v51, v68, v68
	v_add_f32_e32 v91, v69, v91
	v_add_f32_e32 v99, v51, v99
	s_waitcnt vmcnt(6)
	v_lshlrev_b32_e32 v68, 16, v52
	v_and_b32_e32 v52, 0xffff0000, v52
	v_add_f32_e32 v69, v68, v52
	v_mul_f32_e32 v52, v52, v52
	v_fmac_f32_e32 v52, v68, v68
	v_add_f32_e32 v92, 0, v69
	v_lshlrev_b32_e32 v68, 16, v53
	v_and_b32_e32 v53, 0xffff0000, v53
	v_add_f32_e32 v69, v68, v53
	v_mul_f32_e32 v53, v53, v53
	v_fmac_f32_e32 v53, v68, v68
	v_add_f32_e32 v92, v69, v92
	v_add_f32_e32 v100, v52, v53
	v_lshlrev_b32_e32 v68, 16, v54
	v_and_b32_e32 v54, 0xffff0000, v54
	v_add_f32_e32 v69, v68, v54
	v_mul_f32_e32 v54, v54, v54
	v_fmac_f32_e32 v54, v68, v68
	v_add_f32_e32 v92, v69, v92
	v_add_f32_e32 v100, v54, v100
	v_lshlrev_b32_e32 v68, 16, v55
	v_and_b32_e32 v55, 0xffff0000, v55
	v_add_f32_e32 v69, v68, v55
	v_mul_f32_e32 v55, v55, v55
	v_fmac_f32_e32 v55, v68, v68
	v_add_f32_e32 v92, v69, v92
	v_add_f32_e32 v100, v55, v100
	v_lshlrev_b32_e32 v68, 16, v56
	v_and_b32_e32 v56, 0xffff0000, v56
	v_add_f32_e32 v69, v68, v56
	v_mul_f32_e32 v56, v56, v56
	v_fmac_f32_e32 v56, v68, v68
	v_add_f32_e32 v92, v69, v92
	v_add_f32_e32 v100, v56, v100
	v_lshlrev_b32_e32 v68, 16, v57
	v_and_b32_e32 v57, 0xffff0000, v57
	v_add_f32_e32 v69, v68, v57
	v_mul_f32_e32 v57, v57, v57
	v_fmac_f32_e32 v57, v68, v68
	v_add_f32_e32 v92, v69, v92
	v_add_f32_e32 v100, v57, v100
	v_lshlrev_b32_e32 v68, 16, v58
	v_and_b32_e32 v58, 0xffff0000, v58
	v_add_f32_e32 v69, v68, v58
	v_mul_f32_e32 v58, v58, v58
	v_fmac_f32_e32 v58, v68, v68
	v_add_f32_e32 v92, v69, v92
	v_add_f32_e32 v100, v58, v100
	v_lshlrev_b32_e32 v68, 16, v59
	v_and_b32_e32 v59, 0xffff0000, v59
	v_add_f32_e32 v69, v68, v59
	v_mul_f32_e32 v59, v59, v59
	v_fmac_f32_e32 v59, v68, v68
	v_add_f32_e32 v92, v69, v92
	v_add_f32_e32 v100, v59, v100
	s_waitcnt vmcnt(4)
; __device__ __forceinline__ float wave_sum(float v) {
; #pragma unroll
;     for (int o = 1; o < 64; o <<= 1) v += __shfl_xor(v, o);
;     return v;
; __device__ __forceinline__ void unit(LAS unsigned char* lds, const bf16* Z, const bf16* sgw, const float* lng, const float* lnb, const float* sgb, bf16* OBp, int b, int nchunk, int g0, int ng, const int tid_in) {
;     ...
;         for (int q = 0; q < 2; ++q) { const v4u vv = *(const v4u*)(row + q * 512 + lane * 8); const unsigned ww[4] = {vv.x, vv.y, vv.z, vv.w};
; #pragma unroll
;             for (int e = 0; e < 4; ++e) { const float a = bflo(ww[e]), c = bfhi(ww[e]); s += a + c; ss += a * a + c * c; } }
;         s = wave_sum(s); ss = wave_sum(ss);
	v_lshlrev_b32_e32 v68, 16, v60
	v_and_b32_e32 v60, 0xffff0000, v60
	v_add_f32_e32 v69, v68, v60
	v_mul_f32_e32 v60, v60, v60
	v_fmac_f32_e32 v60, v68, v68
	v_add_f32_e32 v93, 0, v69
	v_lshlrev_b32_e32 v68, 16, v61
	v_and_b32_e32 v61, 0xffff0000, v61
	v_add_f32_e32 v69, v68, v61
	v_mul_f32_e32 v61, v61, v61
	v_fmac_f32_e32 v61, v68, v68
	v_add_f32_e32 v93, v69, v93
	v_add_f32_e32 v101, v60, v61
	v_lshlrev_b32_e32 v68, 16, v62
	v_and_b32_e32 v62, 0xffff0000, v62
	v_add_f32_e32 v69, v68, v62
	v_mul_f32_e32 v62, v62, v62
	v_fmac_f32_e32 v62, v68, v68
	v_add_f32_e32 v93, v69, v93
	v_add_f32_e32 v101, v62, v101
	v_lshlrev_b32_e32 v68, 16, v63
	v_and_b32_e32 v63, 0xffff0000, v63
	v_add_f32_e32 v69, v68, v63
	v_mul_f32_e32 v63, v63, v63
	v_fmac_f32_e32 v63, v68, v68
	v_add_f32_e32 v93, v69, v93
	v_add_f32_e32 v101, v63, v101
	v_lshlrev_b32_e32 v68, 16, v64
	v_and_b32_e32 v64, 0xffff0000, v64
	v_add_f32_e32 v69, v68, v64
	v_mul_f32_e32 v64, v64, v64
	v_fmac_f32_e32 v64, v68, v68
	v_add_f32_e32 v93, v69, v93
	v_add_f32_e32 v101, v64, v101
	v_lshlrev_b32_e32 v68, 16, v65
	v_and_b32_e32 v65, 0xffff0000, v65
	v_add_f32_e32 v69, v68, v65
	v_mul_f32_e32 v65, v65, v65
	v_fmac_f32_e32 v65, v68, v68
	v_add_f32_e32 v93, v69, v93
	v_add_f32_e32 v101, v65, v101
	v_lshlrev_b32_e32 v68, 16, v66
	v_and_b32_e32 v66, 0xffff0000, v66
	v_add_f32_e32 v69, v68, v66
	v_mul_f32_e32 v66, v66, v66
	v_fmac_f32_e32 v66, v68, v68
	v_add_f32_e32 v93, v69, v93
	v_add_f32_e32 v101, v66, v101
	v_lshlrev_b32_e32 v68, 16, v67
	v_and_b32_e32 v67, 0xffff0000, v67
	v_add_f32_e32 v69, v68, v67
	v_mul_f32_e32 v67, v67, v67
	v_fmac_f32_e32 v67, v68, v68
	v_add_f32_e32 v93, v69, v93
	v_add_f32_e32 v101, v67, v101
	s_waitcnt vmcnt(2)
	v_lshlrev_b32_e32 v68, 16, v72
	v_and_b32_e32 v72, 0xffff0000, v72
	v_add_f32_e32 v69, v68, v72
	v_mul_f32_e32 v72, v72, v72
	v_fmac_f32_e32 v72, v68, v68
	v_add_f32_e32 v94, 0, v69
	v_lshlrev_b32_e32 v68, 16, v73
	v_and_b32_e32 v73, 0xffff0000, v73
	v_add_f32_e32 v69, v68, v73
	v_mul_f32_e32 v73, v73, v73
	v_fmac_f32_e32 v73, v68, v68
	v_add_f32_e32 v94, v69, v94
	v_add_f32_e32 v102, v72, v73
	v_lshlrev_b32_e32 v68, 16, v74
	v_and_b32_e32 v74, 0xffff0000, v74
	v_add_f32_e32 v69, v68, v74
	v_mul_f32_e32 v74, v74, v74
	v_fmac_f32_e32 v74, v68, v68
	v_add_f32_e32 v94, v69, v94
	v_add_f32_e32 v102, v74, v102
	v_lshlrev_b32_e32 v68, 16, v75
	v_and_b32_e32 v75, 0xffff0000, v75
	v_add_f32_e32 v69, v68, v75
	v_mul_f32_e32 v75, v75, v75
	v_fmac_f32_e32 v75, v68, v68
	v_add_f32_e32 v94, v69, v94
	v_add_f32_e32 v102, v75, v102
	v_lshlrev_b32_e32 v68, 16, v76
	v_and_b32_e32 v76, 0xffff0000, v76
	v_add_f32_e32 v69, v68, v76
	v_mul_f32_e32 v76, v76, v76
	v_fmac_f32_e32 v76, v68, v68
	v_add_f32_e32 v94, v69, v94
	v_add_f32_e32 v102, v76, v102
	v_lshlrev_b32_e32 v68, 16, v77
	v_and_b32_e32 v77, 0xffff0000, v77
	v_add_f32_e32 v69, v68, v77
	v_mul_f32_e32 v77, v77, v77
	v_fmac_f32_e32 v77, v68, v68
	v_add_f32_e32 v94, v69, v94
	v_add_f32_e32 v102, v77, v102
	v_lshlrev_b32_e32 v68, 16, v78
	v_and_b32_e32 v78, 0xffff0000, v78
	v_add_f32_e32 v69, v68, v78
	v_mul_f32_e32 v78, v78, v78
	v_fmac_f32_e32 v78, v68, v68
	v_add_f32_e32 v94, v69, v94
	v_add_f32_e32 v102, v78, v102
	v_lshlrev_b32_e32 v68, 16, v79
	v_and_b32_e32 v79, 0xffff0000, v79
	v_add_f32_e32 v69, v68, v79
	v_mul_f32_e32 v79, v79, v79
	v_fmac_f32_e32 v79, v68, v68
	v_add_f32_e32 v94, v69, v94
	v_add_f32_e32 v102, v79, v102
	s_waitcnt vmcnt(0)
	v_lshlrev_b32_e32 v68, 16, v80
	v_and_b32_e32 v80, 0xffff0000, v80
	v_add_f32_e32 v69, v68, v80
	v_mul_f32_e32 v80, v80, v80
	v_fmac_f32_e32 v80, v68, v68
	v_add_f32_e32 v95, 0, v69
	v_lshlrev_b32_e32 v68, 16, v81
	v_and_b32_e32 v81, 0xffff0000, v81
	v_add_f32_e32 v69, v68, v81
	v_mul_f32_e32 v81, v81, v81
	v_fmac_f32_e32 v81, v68, v68
	v_add_f32_e32 v95, v69, v95
	v_add_f32_e32 v71, v80, v81
	v_lshlrev_b32_e32 v68, 16, v82
	v_and_b32_e32 v82, 0xffff0000, v82
	v_add_f32_e32 v69, v68, v82
	v_mul_f32_e32 v82, v82, v82
	v_fmac_f32_e32 v82, v68, v68
	v_add_f32_e32 v95, v69, v95
	v_add_f32_e32 v71, v82, v71
	v_lshlrev_b32_e32 v68, 16, v83
	v_and_b32_e32 v83, 0xffff0000, v83
	v_add_f32_e32 v69, v68, v83
	v_mul_f32_e32 v83, v83, v83
	v_fmac_f32_e32 v83, v68, v68
	v_add_f32_e32 v95, v69, v95
	v_add_f32_e32 v71, v83, v71
	v_lshlrev_b32_e32 v68, 16, v84
	v_and_b32_e32 v84, 0xffff0000, v84
	v_add_f32_e32 v69, v68, v84
	v_mul_f32_e32 v84, v84, v84
	v_fmac_f32_e32 v84, v68, v68
	v_add_f32_e32 v95, v69, v95
	v_add_f32_e32 v71, v84, v71
	v_lshlrev_b32_e32 v68, 16, v85
	v_and_b32_e32 v85, 0xffff0000, v85
	v_add_f32_e32 v69, v68, v85
	v_mul_f32_e32 v85, v85, v85
	v_fmac_f32_e32 v85, v68, v68
	v_add_f32_e32 v95, v69, v95
	v_add_f32_e32 v71, v85, v71
	v_lshlrev_b32_e32 v68, 16, v86
	v_and_b32_e32 v86, 0xffff0000, v86
	v_add_f32_e32 v69, v68, v86
	v_mul_f32_e32 v86, v86, v86
	v_fmac_f32_e32 v86, v68, v68
	v_add_f32_e32 v95, v69, v95
	v_add_f32_e32 v71, v86, v71
	v_lshlrev_b32_e32 v68, 16, v87
	v_and_b32_e32 v87, 0xffff0000, v87
	v_add_f32_e32 v69, v68, v87
	v_mul_f32_e32 v87, v87, v87
	v_fmac_f32_e32 v87, v68, v68
	v_add_f32_e32 v95, v69, v95
	v_add_f32_e32 v71, v87, v71
	ds_bpermute_b32 v20, v5, v88
	ds_bpermute_b32 v21, v5, v89
	ds_bpermute_b32 v22, v5, v90
	ds_bpermute_b32 v23, v5, v91
	ds_bpermute_b32 v24, v5, v92
	ds_bpermute_b32 v25, v5, v93
	ds_bpermute_b32 v26, v5, v94
	ds_bpermute_b32 v27, v5, v95
	s_waitcnt lgkmcnt(0)
	v_add_f32_e32 v88, v88, v20
	v_add_f32_e32 v89, v89, v21
	v_add_f32_e32 v90, v90, v22
	v_add_f32_e32 v91, v91, v23
	v_add_f32_e32 v92, v92, v24
	v_add_f32_e32 v93, v93, v25
	v_add_f32_e32 v94, v94, v26
	v_add_f32_e32 v95, v95, v27
	ds_bpermute_b32 v20, v5, v96
	ds_bpermute_b32 v21, v5, v97
	ds_bpermute_b32 v22, v5, v98
	ds_bpermute_b32 v23, v5, v99
	ds_bpermute_b32 v24, v5, v100
	ds_bpermute_b32 v25, v5, v101
	ds_bpermute_b32 v26, v5, v102
	ds_bpermute_b32 v27, v5, v71
	s_waitcnt lgkmcnt(0)
; __device__ __forceinline__ float wave_sum(float v) {
; #pragma unroll
;     for (int o = 1; o < 64; o <<= 1) v += __shfl_xor(v, o);
;     return v;
; __device__ __forceinline__ void unit(LAS unsigned char* lds, const bf16* Z, const bf16* sgw, const float* lng, const float* lnb, const float* sgb, bf16* OBp, int b, int nchunk, int g0, int ng, const int tid_in) {
;     ...
;         s = wave_sum(s); ss = wave_sum(ss);
	v_add_f32_e32 v96, v96, v20
	v_add_f32_e32 v97, v97, v21
	v_add_f32_e32 v98, v98, v22
	v_add_f32_e32 v99, v99, v23
	v_add_f32_e32 v100, v100, v24
	v_add_f32_e32 v101, v101, v25
	v_add_f32_e32 v102, v102, v26
	v_add_f32_e32 v71, v71, v27
	ds_bpermute_b32 v20, v6, v88
	ds_bpermute_b32 v21, v6, v89
	ds_bpermute_b32 v22, v6, v90
	ds_bpermute_b32 v23, v6, v91
	ds_bpermute_b32 v24, v6, v92
	ds_bpermute_b32 v25, v6, v93
	ds_bpermute_b32 v26, v6, v94
	ds_bpermute_b32 v27, v6, v95
	s_waitcnt lgkmcnt(0)
	v_add_f32_e32 v88, v88, v20
	v_add_f32_e32 v89, v89, v21
	v_add_f32_e32 v90, v90, v22
	v_add_f32_e32 v91, v91, v23
	v_add_f32_e32 v92, v92, v24
	v_add_f32_e32 v93, v93, v25
	v_add_f32_e32 v94, v94, v26
	v_add_f32_e32 v95, v95, v27
	ds_bpermute_b32 v20, v6, v96
	ds_bpermute_b32 v21, v6, v97
	ds_bpermute_b32 v22, v6, v98
	ds_bpermute_b32 v23, v6, v99
	ds_bpermute_b32 v24, v6, v100
	ds_bpermute_b32 v25, v6, v101
	ds_bpermute_b32 v26, v6, v102
	ds_bpermute_b32 v27, v6, v71
	s_waitcnt lgkmcnt(0)
	v_add_f32_e32 v96, v96, v20
	v_add_f32_e32 v97, v97, v21
	v_add_f32_e32 v98, v98, v22
	v_add_f32_e32 v99, v99, v23
	v_add_f32_e32 v100, v100, v24
	v_add_f32_e32 v101, v101, v25
	v_add_f32_e32 v102, v102, v26
	v_add_f32_e32 v71, v71, v27
	ds_bpermute_b32 v20, v7, v88
	ds_bpermute_b32 v21, v7, v89
	ds_bpermute_b32 v22, v7, v90
	ds_bpermute_b32 v23, v7, v91
	ds_bpermute_b32 v24, v7, v92
	ds_bpermute_b32 v25, v7, v93
	ds_bpermute_b32 v26, v7, v94
	ds_bpermute_b32 v27, v7, v95
	s_waitcnt lgkmcnt(0)
	v_add_f32_e32 v88, v88, v20
	v_add_f32_e32 v89, v89, v21
	v_add_f32_e32 v90, v90, v22
	v_add_f32_e32 v91, v91, v23
	v_add_f32_e32 v92, v92, v24
	v_add_f32_e32 v93, v93, v25
	v_add_f32_e32 v94, v94, v26
	v_add_f32_e32 v95, v95, v27
	ds_bpermute_b32 v20, v7, v96
	ds_bpermute_b32 v21, v7, v97
	ds_bpermute_b32 v22, v7, v98
	ds_bpermute_b32 v23, v7, v99
	ds_bpermute_b32 v24, v7, v100
	ds_bpermute_b32 v25, v7, v101
	ds_bpermute_b32 v26, v7, v102
	ds_bpermute_b32 v27, v7, v71
	s_waitcnt lgkmcnt(0)
	v_add_f32_e32 v96, v96, v20
	v_add_f32_e32 v97, v97, v21
	v_add_f32_e32 v98, v98, v22
	v_add_f32_e32 v99, v99, v23
	v_add_f32_e32 v100, v100, v24
	v_add_f32_e32 v101, v101, v25
	v_add_f32_e32 v102, v102, v26
	v_add_f32_e32 v71, v71, v27
	ds_bpermute_b32 v20, v8, v88
	ds_bpermute_b32 v21, v8, v89
	ds_bpermute_b32 v22, v8, v90
	ds_bpermute_b32 v23, v8, v91
	ds_bpermute_b32 v24, v8, v92
	ds_bpermute_b32 v25, v8, v93
	ds_bpermute_b32 v26, v8, v94
	ds_bpermute_b32 v27, v8, v95
	s_waitcnt lgkmcnt(0)
	v_add_f32_e32 v88, v88, v20
	v_add_f32_e32 v89, v89, v21
	v_add_f32_e32 v90, v90, v22
	v_add_f32_e32 v91, v91, v23
	v_add_f32_e32 v92, v92, v24
	v_add_f32_e32 v93, v93, v25
	v_add_f32_e32 v94, v94, v26
	v_add_f32_e32 v95, v95, v27
	ds_bpermute_b32 v20, v8, v96
	ds_bpermute_b32 v21, v8, v97
	ds_bpermute_b32 v22, v8, v98
	ds_bpermute_b32 v23, v8, v99
	ds_bpermute_b32 v24, v8, v100
	ds_bpermute_b32 v25, v8, v101
	ds_bpermute_b32 v26, v8, v102
	ds_bpermute_b32 v27, v8, v71
	s_waitcnt lgkmcnt(0)
	v_add_f32_e32 v96, v96, v20
	v_add_f32_e32 v97, v97, v21
	v_add_f32_e32 v98, v98, v22
	v_add_f32_e32 v99, v99, v23
	v_add_f32_e32 v100, v100, v24
	v_add_f32_e32 v101, v101, v25
	v_add_f32_e32 v102, v102, v26
	v_add_f32_e32 v71, v71, v27
	ds_bpermute_b32 v20, v9, v88
	ds_bpermute_b32 v21, v9, v89
	ds_bpermute_b32 v22, v9, v90
	ds_bpermute_b32 v23, v9, v91
	ds_bpermute_b32 v24, v9, v92
	ds_bpermute_b32 v25, v9, v93
	ds_bpermute_b32 v26, v9, v94
	ds_bpermute_b32 v27, v9, v95
	s_waitcnt lgkmcnt(0)
	v_add_f32_e32 v88, v88, v20
	v_add_f32_e32 v89, v89, v21
	v_add_f32_e32 v90, v90, v22
	v_add_f32_e32 v91, v91, v23
	v_add_f32_e32 v92, v92, v24
	v_add_f32_e32 v93, v93, v25
	v_add_f32_e32 v94, v94, v26
	v_add_f32_e32 v95, v95, v27
	ds_bpermute_b32 v20, v9, v96
	ds_bpermute_b32 v21, v9, v97
	ds_bpermute_b32 v22, v9, v98
	ds_bpermute_b32 v23, v9, v99
	ds_bpermute_b32 v24, v9, v100
	ds_bpermute_b32 v25, v9, v101
	ds_bpermute_b32 v26, v9, v102
	ds_bpermute_b32 v27, v9, v71
	s_waitcnt lgkmcnt(0)
	v_add_f32_e32 v96, v96, v20
	v_add_f32_e32 v97, v97, v21
	v_add_f32_e32 v98, v98, v22
	v_add_f32_e32 v99, v99, v23
	v_add_f32_e32 v100, v100, v24
	v_add_f32_e32 v101, v101, v25
	v_add_f32_e32 v102, v102, v26
	v_add_f32_e32 v71, v71, v27
	ds_bpermute_b32 v20, v10, v88
	ds_bpermute_b32 v21, v10, v89
	ds_bpermute_b32 v22, v10, v90
	ds_bpermute_b32 v23, v10, v91
	ds_bpermute_b32 v24, v10, v92
	ds_bpermute_b32 v25, v10, v93
	ds_bpermute_b32 v26, v10, v94
	ds_bpermute_b32 v27, v10, v95
	s_waitcnt lgkmcnt(0)
	v_add_f32_e32 v88, v88, v20
	v_add_f32_e32 v89, v89, v21
	v_add_f32_e32 v90, v90, v22
	v_add_f32_e32 v91, v91, v23
	v_add_f32_e32 v92, v92, v24
	v_add_f32_e32 v93, v93, v25
	v_add_f32_e32 v94, v94, v26
	v_add_f32_e32 v95, v95, v27
	ds_bpermute_b32 v20, v10, v96
	ds_bpermute_b32 v21, v10, v97
	ds_bpermute_b32 v22, v10, v98
	ds_bpermute_b32 v23, v10, v99
	ds_bpermute_b32 v24, v10, v100
	ds_bpermute_b32 v25, v10, v101
	ds_bpermute_b32 v26, v10, v102
	ds_bpermute_b32 v27, v10, v71
	s_waitcnt lgkmcnt(0)
	v_add_f32_e32 v96, v96, v20
	v_add_f32_e32 v97, v97, v21
	v_add_f32_e32 v98, v98, v22
	v_add_f32_e32 v99, v99, v23
	v_add_f32_e32 v100, v100, v24
	v_add_f32_e32 v101, v101, v25
	v_add_f32_e32 v102, v102, v26
	v_add_f32_e32 v71, v71, v27
	s_and_saveexec_b64 s[16:17], s[0:1]
	s_cbranch_execz .Lsgu_ln_skip0
; __device__ __forceinline__ void unit(LAS unsigned char* lds, const bf16* Z, const bf16* sgw, const float* lng, const float* lnb, const float* sgb, bf16* OBp, int b, int nchunk, int g0, int ng, const int tid_in) {
;     ...
;         const float mean = s * (1.0f / 1024.0f); const float var = fmaxf(ss * (1.0f / 1024.0f) - mean * mean, 0.f);
;         if (lane == 0) { STAT[tok * 2] = mean; STAT[tok * 2 + 1] = 1.0f / sqrtf(var + EPS); } }
	v_mul_f32_e32 v12, 0x3a800000, v88
	v_mul_f32_e32 v11, v12, v12
	s_mov_b32 s4, 0x3a800000
	v_fma_f32 v11, v96, s4, -v11
	v_max_f32_e32 v11, 0, v11
	v_add_f32_e32 v11, 0x3727c5ac, v11
	s_mov_b32 s4, 0xf800000
	v_mul_f32_e32 v13, 0x4f800000, v11
	v_cmp_gt_f32_e32 vcc, s4, v11
	s_nop 1
	v_cndmask_b32_e32 v11, v11, v13, vcc
	v_sqrt_f32_e32 v13, v11
	s_nop 0
	v_add_u32_e32 v14, -1, v13
	v_fma_f32 v15, -v14, v13, v11
	v_cmp_ge_f32_e64 s[4:5], 0, v15
	v_add_u32_e32 v15, 1, v13
	s_nop 0
	v_cndmask_b32_e64 v14, v13, v14, s[4:5]
	v_fma_f32 v13, -v15, v13, v11
	v_cmp_lt_f32_e64 s[4:5], 0, v13
	s_nop 1
	v_cndmask_b32_e64 v13, v14, v15, s[4:5]
	v_mul_f32_e32 v14, 0x37800000, v13
	v_cndmask_b32_e32 v13, v13, v14, vcc
	v_cmp_class_f32_e32 vcc, v11, v225
	s_nop 1
	v_cndmask_b32_e32 v11, v13, v11, vcc
	v_div_scale_f32 v13, s[4:5], v11, v11, 1.0
	v_rcp_f32_e32 v14, v13
	s_add_i32 s4, s28, 0x19800
	v_fma_f32 v15, -v13, v14, 1.0
	v_fmac_f32_e32 v14, v15, v14
	v_div_scale_f32 v15, vcc, 1.0, v11, 1.0
	v_mul_f32_e32 v16, v15, v14
	v_fma_f32 v17, -v13, v16, v15
	v_fmac_f32_e32 v16, v17, v14
	v_fma_f32 v13, -v13, v16, v15
	s_nop 1
	v_div_fmas_f32 v13, v13, v14, v16
	v_div_fixup_f32 v13, v13, v11, 1.0
	v_mov_b32_e32 v11, s4
	ds_write_b64 v11, v[12:13]
	v_mul_f32_e32 v12, 0x3a800000, v89
	v_mul_f32_e32 v11, v12, v12
	s_mov_b32 s4, 0x3a800000
	v_fma_f32 v11, v97, s4, -v11
	v_max_f32_e32 v11, 0, v11
	v_add_f32_e32 v11, 0x3727c5ac, v11
	s_mov_b32 s4, 0xf800000
	v_mul_f32_e32 v13, 0x4f800000, v11
	v_cmp_gt_f32_e32 vcc, s4, v11
	s_nop 1
	v_cndmask_b32_e32 v11, v11, v13, vcc
	v_sqrt_f32_e32 v13, v11
	s_nop 0
	v_add_u32_e32 v14, -1, v13
	v_fma_f32 v15, -v14, v13, v11
	v_cmp_ge_f32_e64 s[4:5], 0, v15
	v_add_u32_e32 v15, 1, v13
	s_nop 0
	v_cndmask_b32_e64 v14, v13, v14, s[4:5]
	v_fma_f32 v13, -v15, v13, v11
	v_cmp_lt_f32_e64 s[4:5], 0, v13
	s_nop 1
	v_cndmask_b32_e64 v13, v14, v15, s[4:5]
	v_mul_f32_e32 v14, 0x37800000, v13
	v_cndmask_b32_e32 v13, v13, v14, vcc
	v_cmp_class_f32_e32 vcc, v11, v225
	s_nop 1
	v_cndmask_b32_e32 v11, v13, v11, vcc
	v_div_scale_f32 v13, s[4:5], v11, v11, 1.0
	v_rcp_f32_e32 v14, v13
	s_add_i32 s4, s28, 0x19808
	v_fma_f32 v15, -v13, v14, 1.0
	v_fmac_f32_e32 v14, v15, v14
	v_div_scale_f32 v15, vcc, 1.0, v11, 1.0
	v_mul_f32_e32 v16, v15, v14
	v_fma_f32 v17, -v13, v16, v15
	v_fmac_f32_e32 v16, v17, v14
	v_fma_f32 v13, -v13, v16, v15
	s_nop 1
	v_div_fmas_f32 v13, v13, v14, v16
	v_div_fixup_f32 v13, v13, v11, 1.0
	v_mov_b32_e32 v11, s4
	ds_write_b64 v11, v[12:13]
	v_mul_f32_e32 v12, 0x3a800000, v90
	v_mul_f32_e32 v11, v12, v12
	s_mov_b32 s4, 0x3a800000
	v_fma_f32 v11, v98, s4, -v11
	v_max_f32_e32 v11, 0, v11
	v_add_f32_e32 v11, 0x3727c5ac, v11
	s_mov_b32 s4, 0xf800000
	v_mul_f32_e32 v13, 0x4f800000, v11
	v_cmp_gt_f32_e32 vcc, s4, v11
	s_nop 1
	v_cndmask_b32_e32 v11, v11, v13, vcc
	v_sqrt_f32_e32 v13, v11
	s_nop 0
	v_add_u32_e32 v14, -1, v13
	v_fma_f32 v15, -v14, v13, v11
	v_cmp_ge_f32_e64 s[4:5], 0, v15
	v_add_u32_e32 v15, 1, v13
	s_nop 0
	v_cndmask_b32_e64 v14, v13, v14, s[4:5]
	v_fma_f32 v13, -v15, v13, v11
	v_cmp_lt_f32_e64 s[4:5], 0, v13
	s_nop 1
	v_cndmask_b32_e64 v13, v14, v15, s[4:5]
	v_mul_f32_e32 v14, 0x37800000, v13
	v_cndmask_b32_e32 v13, v13, v14, vcc
	v_cmp_class_f32_e32 vcc, v11, v225
	s_nop 1
	v_cndmask_b32_e32 v11, v13, v11, vcc
	v_div_scale_f32 v13, s[4:5], v11, v11, 1.0
	v_rcp_f32_e32 v14, v13
	s_add_i32 s4, s28, 0x19810
	v_fma_f32 v15, -v13, v14, 1.0
	v_fmac_f32_e32 v14, v15, v14
	v_div_scale_f32 v15, vcc, 1.0, v11, 1.0
	v_mul_f32_e32 v16, v15, v14
	v_fma_f32 v17, -v13, v16, v15
	v_fmac_f32_e32 v16, v17, v14
	v_fma_f32 v13, -v13, v16, v15
	s_nop 1
	v_div_fmas_f32 v13, v13, v14, v16
	v_div_fixup_f32 v13, v13, v11, 1.0
	v_mov_b32_e32 v11, s4
	ds_write_b64 v11, v[12:13]
	v_mul_f32_e32 v12, 0x3a800000, v91
	v_mul_f32_e32 v11, v12, v12
	s_mov_b32 s4, 0x3a800000
	v_fma_f32 v11, v99, s4, -v11
	v_max_f32_e32 v11, 0, v11
	v_add_f32_e32 v11, 0x3727c5ac, v11
	s_mov_b32 s4, 0xf800000
	v_mul_f32_e32 v13, 0x4f800000, v11
	v_cmp_gt_f32_e32 vcc, s4, v11
	s_nop 1
	v_cndmask_b32_e32 v11, v11, v13, vcc
	v_sqrt_f32_e32 v13, v11
	s_nop 0
	v_add_u32_e32 v14, -1, v13
	v_fma_f32 v15, -v14, v13, v11
	v_cmp_ge_f32_e64 s[4:5], 0, v15
	v_add_u32_e32 v15, 1, v13
	s_nop 0
	v_cndmask_b32_e64 v14, v13, v14, s[4:5]
	v_fma_f32 v13, -v15, v13, v11
	v_cmp_lt_f32_e64 s[4:5], 0, v13
	s_nop 1
	v_cndmask_b32_e64 v13, v14, v15, s[4:5]
	v_mul_f32_e32 v14, 0x37800000, v13
	v_cndmask_b32_e32 v13, v13, v14, vcc
	v_cmp_class_f32_e32 vcc, v11, v225
	s_nop 1
	v_cndmask_b32_e32 v11, v13, v11, vcc
	v_div_scale_f32 v13, s[4:5], v11, v11, 1.0
	v_rcp_f32_e32 v14, v13
	s_add_i32 s4, s28, 0x19818
	v_fma_f32 v15, -v13, v14, 1.0
	v_fmac_f32_e32 v14, v15, v14
	v_div_scale_f32 v15, vcc, 1.0, v11, 1.0
	v_mul_f32_e32 v16, v15, v14
	v_fma_f32 v17, -v13, v16, v15
	v_fmac_f32_e32 v16, v17, v14
	v_fma_f32 v13, -v13, v16, v15
	s_nop 1
	v_div_fmas_f32 v13, v13, v14, v16
	v_div_fixup_f32 v13, v13, v11, 1.0
	v_mov_b32_e32 v11, s4
	ds_write_b64 v11, v[12:13]
	v_mul_f32_e32 v12, 0x3a800000, v92
	v_mul_f32_e32 v11, v12, v12
	s_mov_b32 s4, 0x3a800000
	v_fma_f32 v11, v100, s4, -v11
	v_max_f32_e32 v11, 0, v11
	v_add_f32_e32 v11, 0x3727c5ac, v11
	s_mov_b32 s4, 0xf800000
	v_mul_f32_e32 v13, 0x4f800000, v11
	v_cmp_gt_f32_e32 vcc, s4, v11
	s_nop 1
	v_cndmask_b32_e32 v11, v11, v13, vcc
	v_sqrt_f32_e32 v13, v11
	s_nop 0
	v_add_u32_e32 v14, -1, v13
	v_fma_f32 v15, -v14, v13, v11
	v_cmp_ge_f32_e64 s[4:5], 0, v15
	v_add_u32_e32 v15, 1, v13
	s_nop 0
	v_cndmask_b32_e64 v14, v13, v14, s[4:5]
	v_fma_f32 v13, -v15, v13, v11
	v_cmp_lt_f32_e64 s[4:5], 0, v13
	s_nop 1
	v_cndmask_b32_e64 v13, v14, v15, s[4:5]
; __device__ __forceinline__ void unit(LAS unsigned char* lds, const bf16* Z, const bf16* sgw, const float* lng, const float* lnb, const float* sgb, bf16* OBp, int b, int nchunk, int g0, int ng, const int tid_in) {
;     ...
;         const float mean = s * (1.0f / 1024.0f); const float var = fmaxf(ss * (1.0f / 1024.0f) - mean * mean, 0.f);
;         if (lane == 0) { STAT[tok * 2] = mean; STAT[tok * 2 + 1] = 1.0f / sqrtf(var + EPS); } }
	v_mul_f32_e32 v14, 0x37800000, v13
	v_cndmask_b32_e32 v13, v13, v14, vcc
	v_cmp_class_f32_e32 vcc, v11, v225
	s_nop 1
	v_cndmask_b32_e32 v11, v13, v11, vcc
	v_div_scale_f32 v13, s[4:5], v11, v11, 1.0
	v_rcp_f32_e32 v14, v13
	s_add_i32 s4, s28, 0x19820
	v_fma_f32 v15, -v13, v14, 1.0
	v_fmac_f32_e32 v14, v15, v14
	v_div_scale_f32 v15, vcc, 1.0, v11, 1.0
	v_mul_f32_e32 v16, v15, v14
	v_fma_f32 v17, -v13, v16, v15
	v_fmac_f32_e32 v16, v17, v14
	v_fma_f32 v13, -v13, v16, v15
	s_nop 1
	v_div_fmas_f32 v13, v13, v14, v16
	v_div_fixup_f32 v13, v13, v11, 1.0
	v_mov_b32_e32 v11, s4
	ds_write_b64 v11, v[12:13]
	v_mul_f32_e32 v12, 0x3a800000, v93
	v_mul_f32_e32 v11, v12, v12
	s_mov_b32 s4, 0x3a800000
	v_fma_f32 v11, v101, s4, -v11
	v_max_f32_e32 v11, 0, v11
	v_add_f32_e32 v11, 0x3727c5ac, v11
	s_mov_b32 s4, 0xf800000
	v_mul_f32_e32 v13, 0x4f800000, v11
	v_cmp_gt_f32_e32 vcc, s4, v11
	s_nop 1
	v_cndmask_b32_e32 v11, v11, v13, vcc
	v_sqrt_f32_e32 v13, v11
	s_nop 0
	v_add_u32_e32 v14, -1, v13
	v_fma_f32 v15, -v14, v13, v11
	v_cmp_ge_f32_e64 s[4:5], 0, v15
	v_add_u32_e32 v15, 1, v13
	s_nop 0
	v_cndmask_b32_e64 v14, v13, v14, s[4:5]
	v_fma_f32 v13, -v15, v13, v11
	v_cmp_lt_f32_e64 s[4:5], 0, v13
	s_nop 1
	v_cndmask_b32_e64 v13, v14, v15, s[4:5]
	v_mul_f32_e32 v14, 0x37800000, v13
	v_cndmask_b32_e32 v13, v13, v14, vcc
	v_cmp_class_f32_e32 vcc, v11, v225
	s_nop 1
	v_cndmask_b32_e32 v11, v13, v11, vcc
	v_div_scale_f32 v13, s[4:5], v11, v11, 1.0
	v_rcp_f32_e32 v14, v13
	s_add_i32 s4, s28, 0x19828
	v_fma_f32 v15, -v13, v14, 1.0
	v_fmac_f32_e32 v14, v15, v14
	v_div_scale_f32 v15, vcc, 1.0, v11, 1.0
	v_mul_f32_e32 v16, v15, v14
	v_fma_f32 v17, -v13, v16, v15
	v_fmac_f32_e32 v16, v17, v14
	v_fma_f32 v13, -v13, v16, v15
	s_nop 1
	v_div_fmas_f32 v13, v13, v14, v16
	v_div_fixup_f32 v13, v13, v11, 1.0
	v_mov_b32_e32 v11, s4
	ds_write_b64 v11, v[12:13]
	v_mul_f32_e32 v12, 0x3a800000, v94
	v_mul_f32_e32 v11, v12, v12
	s_mov_b32 s4, 0x3a800000
	v_fma_f32 v11, v102, s4, -v11
	v_max_f32_e32 v11, 0, v11
	v_add_f32_e32 v11, 0x3727c5ac, v11
	s_mov_b32 s4, 0xf800000
	v_mul_f32_e32 v13, 0x4f800000, v11
	v_cmp_gt_f32_e32 vcc, s4, v11
	s_nop 1
	v_cndmask_b32_e32 v11, v11, v13, vcc
	v_sqrt_f32_e32 v13, v11
	s_nop 0
	v_add_u32_e32 v14, -1, v13
	v_fma_f32 v15, -v14, v13, v11
	v_cmp_ge_f32_e64 s[4:5], 0, v15
	v_add_u32_e32 v15, 1, v13
	s_nop 0
	v_cndmask_b32_e64 v14, v13, v14, s[4:5]
	v_fma_f32 v13, -v15, v13, v11
	v_cmp_lt_f32_e64 s[4:5], 0, v13
	s_nop 1
	v_cndmask_b32_e64 v13, v14, v15, s[4:5]
	v_mul_f32_e32 v14, 0x37800000, v13
	v_cndmask_b32_e32 v13, v13, v14, vcc
	v_cmp_class_f32_e32 vcc, v11, v225
	s_nop 1
	v_cndmask_b32_e32 v11, v13, v11, vcc
	v_div_scale_f32 v13, s[4:5], v11, v11, 1.0
	v_rcp_f32_e32 v14, v13
	s_add_i32 s4, s28, 0x19830
	v_fma_f32 v15, -v13, v14, 1.0
	v_fmac_f32_e32 v14, v15, v14
	v_div_scale_f32 v15, vcc, 1.0, v11, 1.0
	v_mul_f32_e32 v16, v15, v14
	v_fma_f32 v17, -v13, v16, v15
	v_fmac_f32_e32 v16, v17, v14
	v_fma_f32 v13, -v13, v16, v15
	s_nop 1
	v_div_fmas_f32 v13, v13, v14, v16
	v_div_fixup_f32 v13, v13, v11, 1.0
	v_mov_b32_e32 v11, s4
	ds_write_b64 v11, v[12:13]
	v_mul_f32_e32 v12, 0x3a800000, v95
	v_mul_f32_e32 v11, v12, v12
	s_mov_b32 s4, 0x3a800000
	v_fma_f32 v11, v71, s4, -v11
	v_max_f32_e32 v11, 0, v11
	v_add_f32_e32 v11, 0x3727c5ac, v11
	s_mov_b32 s4, 0xf800000
	v_mul_f32_e32 v13, 0x4f800000, v11
	v_cmp_gt_f32_e32 vcc, s4, v11
	s_nop 1
	v_cndmask_b32_e32 v11, v11, v13, vcc
	v_sqrt_f32_e32 v13, v11
	s_nop 0
	v_add_u32_e32 v14, -1, v13
	v_fma_f32 v15, -v14, v13, v11
	v_cmp_ge_f32_e64 s[4:5], 0, v15
	v_add_u32_e32 v15, 1, v13
	s_nop 0
	v_cndmask_b32_e64 v14, v13, v14, s[4:5]
	v_fma_f32 v13, -v15, v13, v11
	v_cmp_lt_f32_e64 s[4:5], 0, v13
	s_nop 1
	v_cndmask_b32_e64 v13, v14, v15, s[4:5]
	v_mul_f32_e32 v14, 0x37800000, v13
	v_cndmask_b32_e32 v13, v13, v14, vcc
	v_cmp_class_f32_e32 vcc, v11, v225
	s_nop 1
	v_cndmask_b32_e32 v11, v13, v11, vcc
	v_div_scale_f32 v13, s[4:5], v11, v11, 1.0
	v_rcp_f32_e32 v14, v13
	s_add_i32 s4, s28, 0x19838
	v_fma_f32 v15, -v13, v14, 1.0
	v_fmac_f32_e32 v14, v15, v14
	v_div_scale_f32 v15, vcc, 1.0, v11, 1.0
	v_mul_f32_e32 v16, v15, v14
	v_fma_f32 v17, -v13, v16, v15
	v_fmac_f32_e32 v16, v17, v14
	v_fma_f32 v13, -v13, v16, v15
	s_nop 1
	v_div_fmas_f32 v13, v13, v14, v16
	v_div_fixup_f32 v13, v13, v11, 1.0
	v_mov_b32_e32 v11, s4
	ds_write_b64 v11, v[12:13]
; __device__ __forceinline__ void unit(LAS unsigned char* lds, const bf16* Z, const bf16* sgw, const float* lng, const float* lnb, const float* sgb, bf16* OBp, int b, int nchunk, int g0, int ng, const int tid_in) {
;     ...
;     for (int k = 0; k < 16; ++k) { const int tok = 16 * w + k; const bf16* row = Z + (size_t)(tb0 + tok) * ZLD + ZV;
;         float s = 0.f, ss = 0.f;
; #pragma unroll
;         for (int q = 0; q < 2; ++q) { const v4u vv = *(const v4u*)(row + q * 512 + lane * 8); const unsigned ww[4] = {vv.x, vv.y, vv.z, vv.w};
; #pragma unroll
;             for (int e = 0; e < 4; ++e) { const float a = bflo(ww[e]), c = bfhi(ww[e]); s += a + c; ss += a * a + c * c; } }
.Lsgu_ln_skip0:
	s_or_b64 exec, exec, s[16:17]
	s_mov_b64 s[4:5], 0x4600
	global_load_dwordx4 v[20:23], v[2:3], off
	global_load_dwordx4 v[24:27], v[2:3], off offset:1024
	v_lshl_add_u64 v[2:3], v[2:3], 0, s[4:5]
	global_load_dwordx4 v[28:31], v[2:3], off
	global_load_dwordx4 v[32:35], v[2:3], off offset:1024
	v_lshl_add_u64 v[2:3], v[2:3], 0, s[4:5]
	global_load_dwordx4 v[36:39], v[2:3], off
	global_load_dwordx4 v[40:43], v[2:3], off offset:1024
	v_lshl_add_u64 v[2:3], v[2:3], 0, s[4:5]
	global_load_dwordx4 v[44:47], v[2:3], off
	global_load_dwordx4 v[48:51], v[2:3], off offset:1024
	v_lshl_add_u64 v[2:3], v[2:3], 0, s[4:5]
	global_load_dwordx4 v[52:55], v[2:3], off
	global_load_dwordx4 v[56:59], v[2:3], off offset:1024
	v_lshl_add_u64 v[2:3], v[2:3], 0, s[4:5]
	global_load_dwordx4 v[60:63], v[2:3], off
	global_load_dwordx4 v[64:67], v[2:3], off offset:1024
	v_lshl_add_u64 v[2:3], v[2:3], 0, s[4:5]
	global_load_dwordx4 v[72:75], v[2:3], off
	global_load_dwordx4 v[76:79], v[2:3], off offset:1024
	v_lshl_add_u64 v[2:3], v[2:3], 0, s[4:5]
	global_load_dwordx4 v[80:83], v[2:3], off
	global_load_dwordx4 v[84:87], v[2:3], off offset:1024
	v_lshl_add_u64 v[2:3], v[2:3], 0, s[4:5]
	s_waitcnt vmcnt(14)
	v_lshlrev_b32_e32 v68, 16, v20
	v_and_b32_e32 v20, 0xffff0000, v20
	v_add_f32_e32 v69, v68, v20
	v_mul_f32_e32 v20, v20, v20
	v_fmac_f32_e32 v20, v68, v68
	v_add_f32_e32 v88, 0, v69
	v_lshlrev_b32_e32 v68, 16, v21
	v_and_b32_e32 v21, 0xffff0000, v21
	v_add_f32_e32 v69, v68, v21
	v_mul_f32_e32 v21, v21, v21
	v_fmac_f32_e32 v21, v68, v68
	v_add_f32_e32 v88, v69, v88
	v_add_f32_e32 v96, v20, v21
	v_lshlrev_b32_e32 v68, 16, v22
	v_and_b32_e32 v22, 0xffff0000, v22
	v_add_f32_e32 v69, v68, v22
	v_mul_f32_e32 v22, v22, v22
	v_fmac_f32_e32 v22, v68, v68
	v_add_f32_e32 v88, v69, v88
	v_add_f32_e32 v96, v22, v96
	v_lshlrev_b32_e32 v68, 16, v23
	v_and_b32_e32 v23, 0xffff0000, v23
	v_add_f32_e32 v69, v68, v23
	v_mul_f32_e32 v23, v23, v23
	v_fmac_f32_e32 v23, v68, v68
	v_add_f32_e32 v88, v69, v88
	v_add_f32_e32 v96, v23, v96
	v_lshlrev_b32_e32 v68, 16, v24
	v_and_b32_e32 v24, 0xffff0000, v24
	v_add_f32_e32 v69, v68, v24
	v_mul_f32_e32 v24, v24, v24
	v_fmac_f32_e32 v24, v68, v68
	v_add_f32_e32 v88, v69, v88
	v_add_f32_e32 v96, v24, v96
	v_lshlrev_b32_e32 v68, 16, v25
	v_and_b32_e32 v25, 0xffff0000, v25
	v_add_f32_e32 v69, v68, v25
	v_mul_f32_e32 v25, v25, v25
	v_fmac_f32_e32 v25, v68, v68
	v_add_f32_e32 v88, v69, v88
	v_add_f32_e32 v96, v25, v96
	v_lshlrev_b32_e32 v68, 16, v26
	v_and_b32_e32 v26, 0xffff0000, v26
	v_add_f32_e32 v69, v68, v26
	v_mul_f32_e32 v26, v26, v26
	v_fmac_f32_e32 v26, v68, v68
	v_add_f32_e32 v88, v69, v88
	v_add_f32_e32 v96, v26, v96
	v_lshlrev_b32_e32 v68, 16, v27
	v_and_b32_e32 v27, 0xffff0000, v27
	v_add_f32_e32 v69, v68, v27
	v_mul_f32_e32 v27, v27, v27
	v_fmac_f32_e32 v27, v68, v68
	v_add_f32_e32 v88, v69, v88
	v_add_f32_e32 v96, v27, v96
	s_waitcnt vmcnt(12)
	v_lshlrev_b32_e32 v68, 16, v28
	v_and_b32_e32 v28, 0xffff0000, v28
	v_add_f32_e32 v69, v68, v28
	v_mul_f32_e32 v28, v28, v28
	v_fmac_f32_e32 v28, v68, v68
	v_add_f32_e32 v89, 0, v69
	v_lshlrev_b32_e32 v68, 16, v29
	v_and_b32_e32 v29, 0xffff0000, v29
	v_add_f32_e32 v69, v68, v29
	v_mul_f32_e32 v29, v29, v29
	v_fmac_f32_e32 v29, v68, v68
	v_add_f32_e32 v89, v69, v89
	v_add_f32_e32 v97, v28, v29
	v_lshlrev_b32_e32 v68, 16, v30
	v_and_b32_e32 v30, 0xffff0000, v30
	v_add_f32_e32 v69, v68, v30
	v_mul_f32_e32 v30, v30, v30
	v_fmac_f32_e32 v30, v68, v68
	v_add_f32_e32 v89, v69, v89
	v_add_f32_e32 v97, v30, v97
	v_lshlrev_b32_e32 v68, 16, v31
	v_and_b32_e32 v31, 0xffff0000, v31
	v_add_f32_e32 v69, v68, v31
	v_mul_f32_e32 v31, v31, v31
	v_fmac_f32_e32 v31, v68, v68
	v_add_f32_e32 v89, v69, v89
	v_add_f32_e32 v97, v31, v97
	v_lshlrev_b32_e32 v68, 16, v32
	v_and_b32_e32 v32, 0xffff0000, v32
	v_add_f32_e32 v69, v68, v32
	v_mul_f32_e32 v32, v32, v32
	v_fmac_f32_e32 v32, v68, v68
	v_add_f32_e32 v89, v69, v89
	v_add_f32_e32 v97, v32, v97
	v_lshlrev_b32_e32 v68, 16, v33
	v_and_b32_e32 v33, 0xffff0000, v33
	v_add_f32_e32 v69, v68, v33
	v_mul_f32_e32 v33, v33, v33
	v_fmac_f32_e32 v33, v68, v68
	v_add_f32_e32 v89, v69, v89
	v_add_f32_e32 v97, v33, v97
	v_lshlrev_b32_e32 v68, 16, v34
	v_and_b32_e32 v34, 0xffff0000, v34
	v_add_f32_e32 v69, v68, v34
	v_mul_f32_e32 v34, v34, v34
	v_fmac_f32_e32 v34, v68, v68
	v_add_f32_e32 v89, v69, v89
	v_add_f32_e32 v97, v34, v97
	v_lshlrev_b32_e32 v68, 16, v35
	v_and_b32_e32 v35, 0xffff0000, v35
	v_add_f32_e32 v69, v68, v35
	v_mul_f32_e32 v35, v35, v35
	v_fmac_f32_e32 v35, v68, v68
	v_add_f32_e32 v89, v69, v89
	v_add_f32_e32 v97, v35, v97
	s_waitcnt vmcnt(10)
	v_lshlrev_b32_e32 v68, 16, v36
	v_and_b32_e32 v36, 0xffff0000, v36
	v_add_f32_e32 v69, v68, v36
	v_mul_f32_e32 v36, v36, v36
	v_fmac_f32_e32 v36, v68, v68
	v_add_f32_e32 v90, 0, v69
	v_lshlrev_b32_e32 v68, 16, v37
	v_and_b32_e32 v37, 0xffff0000, v37
	v_add_f32_e32 v69, v68, v37
	v_mul_f32_e32 v37, v37, v37
	v_fmac_f32_e32 v37, v68, v68
	v_add_f32_e32 v90, v69, v90
	v_add_f32_e32 v98, v36, v37
	v_lshlrev_b32_e32 v68, 16, v38
	v_and_b32_e32 v38, 0xffff0000, v38
	v_add_f32_e32 v69, v68, v38
	v_mul_f32_e32 v38, v38, v38
	v_fmac_f32_e32 v38, v68, v68
	v_add_f32_e32 v90, v69, v90
	v_add_f32_e32 v98, v38, v98
	v_lshlrev_b32_e32 v68, 16, v39
	v_and_b32_e32 v39, 0xffff0000, v39
	v_add_f32_e32 v69, v68, v39
	v_mul_f32_e32 v39, v39, v39
	v_fmac_f32_e32 v39, v68, v68
	v_add_f32_e32 v90, v69, v90
	v_add_f32_e32 v98, v39, v98
	v_lshlrev_b32_e32 v68, 16, v40
	v_and_b32_e32 v40, 0xffff0000, v40
	v_add_f32_e32 v69, v68, v40
	v_mul_f32_e32 v40, v40, v40
	v_fmac_f32_e32 v40, v68, v68
	v_add_f32_e32 v90, v69, v90
	v_add_f32_e32 v98, v40, v98
	v_lshlrev_b32_e32 v68, 16, v41
	v_and_b32_e32 v41, 0xffff0000, v41
	v_add_f32_e32 v69, v68, v41
	v_mul_f32_e32 v41, v41, v41
	v_fmac_f32_e32 v41, v68, v68
	v_add_f32_e32 v90, v69, v90
	v_add_f32_e32 v98, v41, v98
	v_lshlrev_b32_e32 v68, 16, v42
	v_and_b32_e32 v42, 0xffff0000, v42
	v_add_f32_e32 v69, v68, v42
	v_mul_f32_e32 v42, v42, v42
	v_fmac_f32_e32 v42, v68, v68
	v_add_f32_e32 v90, v69, v90
	v_add_f32_e32 v98, v42, v98
	v_lshlrev_b32_e32 v68, 16, v43
	v_and_b32_e32 v43, 0xffff0000, v43
	v_add_f32_e32 v69, v68, v43
	v_mul_f32_e32 v43, v43, v43
	v_fmac_f32_e32 v43, v68, v68
	v_add_f32_e32 v90, v69, v90
	v_add_f32_e32 v98, v43, v98
	s_waitcnt vmcnt(8)
; __device__ __forceinline__ void unit(LAS unsigned char* lds, const bf16* Z, const bf16* sgw, const float* lng, const float* lnb, const float* sgb, bf16* OBp, int b, int nchunk, int g0, int ng, const int tid_in) {
;     ...
;         for (int q = 0; q < 2; ++q) { const v4u vv = *(const v4u*)(row + q * 512 + lane * 8); const unsigned ww[4] = {vv.x, vv.y, vv.z, vv.w};
; #pragma unroll
;             for (int e = 0; e < 4; ++e) { const float a = bflo(ww[e]), c = bfhi(ww[e]); s += a + c; ss += a * a + c * c; } }
	v_lshlrev_b32_e32 v68, 16, v44
	v_and_b32_e32 v44, 0xffff0000, v44
	v_add_f32_e32 v69, v68, v44
	v_mul_f32_e32 v44, v44, v44
	v_fmac_f32_e32 v44, v68, v68
	v_add_f32_e32 v91, 0, v69
	v_lshlrev_b32_e32 v68, 16, v45
	v_and_b32_e32 v45, 0xffff0000, v45
	v_add_f32_e32 v69, v68, v45
	v_mul_f32_e32 v45, v45, v45
	v_fmac_f32_e32 v45, v68, v68
	v_add_f32_e32 v91, v69, v91
	v_add_f32_e32 v99, v44, v45
	v_lshlrev_b32_e32 v68, 16, v46
	v_and_b32_e32 v46, 0xffff0000, v46
	v_add_f32_e32 v69, v68, v46
	v_mul_f32_e32 v46, v46, v46
	v_fmac_f32_e32 v46, v68, v68
	v_add_f32_e32 v91, v69, v91
	v_add_f32_e32 v99, v46, v99
	v_lshlrev_b32_e32 v68, 16, v47
	v_and_b32_e32 v47, 0xffff0000, v47
	v_add_f32_e32 v69, v68, v47
	v_mul_f32_e32 v47, v47, v47
	v_fmac_f32_e32 v47, v68, v68
	v_add_f32_e32 v91, v69, v91
	v_add_f32_e32 v99, v47, v99
	v_lshlrev_b32_e32 v68, 16, v48
	v_and_b32_e32 v48, 0xffff0000, v48
	v_add_f32_e32 v69, v68, v48
	v_mul_f32_e32 v48, v48, v48
	v_fmac_f32_e32 v48, v68, v68
	v_add_f32_e32 v91, v69, v91
	v_add_f32_e32 v99, v48, v99
	v_lshlrev_b32_e32 v68, 16, v49
	v_and_b32_e32 v49, 0xffff0000, v49
	v_add_f32_e32 v69, v68, v49
	v_mul_f32_e32 v49, v49, v49
	v_fmac_f32_e32 v49, v68, v68
	v_add_f32_e32 v91, v69, v91
	v_add_f32_e32 v99, v49, v99
	v_lshlrev_b32_e32 v68, 16, v50
	v_and_b32_e32 v50, 0xffff0000, v50
	v_add_f32_e32 v69, v68, v50
	v_mul_f32_e32 v50, v50, v50
	v_fmac_f32_e32 v50, v68, v68
	v_add_f32_e32 v91, v69, v91
	v_add_f32_e32 v99, v50, v99
	v_lshlrev_b32_e32 v68, 16, v51
	v_and_b32_e32 v51, 0xffff0000, v51
	v_add_f32_e32 v69, v68, v51
	v_mul_f32_e32 v51, v51, v51
	v_fmac_f32_e32 v51, v68, v68
	v_add_f32_e32 v91, v69, v91
	v_add_f32_e32 v99, v51, v99
	s_waitcnt vmcnt(6)
	v_lshlrev_b32_e32 v68, 16, v52
	v_and_b32_e32 v52, 0xffff0000, v52
	v_add_f32_e32 v69, v68, v52
	v_mul_f32_e32 v52, v52, v52
	v_fmac_f32_e32 v52, v68, v68
	v_add_f32_e32 v92, 0, v69
	v_lshlrev_b32_e32 v68, 16, v53
	v_and_b32_e32 v53, 0xffff0000, v53
	v_add_f32_e32 v69, v68, v53
	v_mul_f32_e32 v53, v53, v53
	v_fmac_f32_e32 v53, v68, v68
	v_add_f32_e32 v92, v69, v92
	v_add_f32_e32 v100, v52, v53
	v_lshlrev_b32_e32 v68, 16, v54
	v_and_b32_e32 v54, 0xffff0000, v54
	v_add_f32_e32 v69, v68, v54
	v_mul_f32_e32 v54, v54, v54
	v_fmac_f32_e32 v54, v68, v68
	v_add_f32_e32 v92, v69, v92
	v_add_f32_e32 v100, v54, v100
	v_lshlrev_b32_e32 v68, 16, v55
	v_and_b32_e32 v55, 0xffff0000, v55
	v_add_f32_e32 v69, v68, v55
	v_mul_f32_e32 v55, v55, v55
	v_fmac_f32_e32 v55, v68, v68
	v_add_f32_e32 v92, v69, v92
	v_add_f32_e32 v100, v55, v100
	v_lshlrev_b32_e32 v68, 16, v56
	v_and_b32_e32 v56, 0xffff0000, v56
	v_add_f32_e32 v69, v68, v56
	v_mul_f32_e32 v56, v56, v56
	v_fmac_f32_e32 v56, v68, v68
	v_add_f32_e32 v92, v69, v92
	v_add_f32_e32 v100, v56, v100
	v_lshlrev_b32_e32 v68, 16, v57
	v_and_b32_e32 v57, 0xffff0000, v57
	v_add_f32_e32 v69, v68, v57
	v_mul_f32_e32 v57, v57, v57
	v_fmac_f32_e32 v57, v68, v68
	v_add_f32_e32 v92, v69, v92
	v_add_f32_e32 v100, v57, v100
	v_lshlrev_b32_e32 v68, 16, v58
	v_and_b32_e32 v58, 0xffff0000, v58
	v_add_f32_e32 v69, v68, v58
	v_mul_f32_e32 v58, v58, v58
	v_fmac_f32_e32 v58, v68, v68
	v_add_f32_e32 v92, v69, v92
	v_add_f32_e32 v100, v58, v100
	v_lshlrev_b32_e32 v68, 16, v59
	v_and_b32_e32 v59, 0xffff0000, v59
	v_add_f32_e32 v69, v68, v59
	v_mul_f32_e32 v59, v59, v59
	v_fmac_f32_e32 v59, v68, v68
	v_add_f32_e32 v92, v69, v92
	v_add_f32_e32 v100, v59, v100
	s_waitcnt vmcnt(4)
	v_lshlrev_b32_e32 v68, 16, v60
	v_and_b32_e32 v60, 0xffff0000, v60
	v_add_f32_e32 v69, v68, v60
	v_mul_f32_e32 v60, v60, v60
	v_fmac_f32_e32 v60, v68, v68
	v_add_f32_e32 v93, 0, v69
	v_lshlrev_b32_e32 v68, 16, v61
	v_and_b32_e32 v61, 0xffff0000, v61
	v_add_f32_e32 v69, v68, v61
	v_mul_f32_e32 v61, v61, v61
	v_fmac_f32_e32 v61, v68, v68
	v_add_f32_e32 v93, v69, v93
	v_add_f32_e32 v101, v60, v61
	v_lshlrev_b32_e32 v68, 16, v62
	v_and_b32_e32 v62, 0xffff0000, v62
	v_add_f32_e32 v69, v68, v62
	v_mul_f32_e32 v62, v62, v62
	v_fmac_f32_e32 v62, v68, v68
	v_add_f32_e32 v93, v69, v93
	v_add_f32_e32 v101, v62, v101
	v_lshlrev_b32_e32 v68, 16, v63
	v_and_b32_e32 v63, 0xffff0000, v63
	v_add_f32_e32 v69, v68, v63
	v_mul_f32_e32 v63, v63, v63
	v_fmac_f32_e32 v63, v68, v68
	v_add_f32_e32 v93, v69, v93
	v_add_f32_e32 v101, v63, v101
	v_lshlrev_b32_e32 v68, 16, v64
	v_and_b32_e32 v64, 0xffff0000, v64
	v_add_f32_e32 v69, v68, v64
	v_mul_f32_e32 v64, v64, v64
	v_fmac_f32_e32 v64, v68, v68
	v_add_f32_e32 v93, v69, v93
	v_add_f32_e32 v101, v64, v101
	v_lshlrev_b32_e32 v68, 16, v65
	v_and_b32_e32 v65, 0xffff0000, v65
	v_add_f32_e32 v69, v68, v65
	v_mul_f32_e32 v65, v65, v65
	v_fmac_f32_e32 v65, v68, v68
	v_add_f32_e32 v93, v69, v93
	v_add_f32_e32 v101, v65, v101
	v_lshlrev_b32_e32 v68, 16, v66
	v_and_b32_e32 v66, 0xffff0000, v66
	v_add_f32_e32 v69, v68, v66
	v_mul_f32_e32 v66, v66, v66
	v_fmac_f32_e32 v66, v68, v68
	v_add_f32_e32 v93, v69, v93
	v_add_f32_e32 v101, v66, v101
	v_lshlrev_b32_e32 v68, 16, v67
	v_and_b32_e32 v67, 0xffff0000, v67
	v_add_f32_e32 v69, v68, v67
	v_mul_f32_e32 v67, v67, v67
	v_fmac_f32_e32 v67, v68, v68
	v_add_f32_e32 v93, v69, v93
	v_add_f32_e32 v101, v67, v101
	s_waitcnt vmcnt(2)
; __device__ __forceinline__ float wave_sum(float v) {
; #pragma unroll
;     for (int o = 1; o < 64; o <<= 1) v += __shfl_xor(v, o);
;     return v;
; __device__ __forceinline__ void unit(LAS unsigned char* lds, const bf16* Z, const bf16* sgw, const float* lng, const float* lnb, const float* sgb, bf16* OBp, int b, int nchunk, int g0, int ng, const int tid_in) {
;     ...
;         for (int q = 0; q < 2; ++q) { const v4u vv = *(const v4u*)(row + q * 512 + lane * 8); const unsigned ww[4] = {vv.x, vv.y, vv.z, vv.w};
; #pragma unroll
;             for (int e = 0; e < 4; ++e) { const float a = bflo(ww[e]), c = bfhi(ww[e]); s += a + c; ss += a * a + c * c; } }
;         s = wave_sum(s); ss = wave_sum(ss);
	v_lshlrev_b32_e32 v68, 16, v72
	v_and_b32_e32 v72, 0xffff0000, v72
	v_add_f32_e32 v69, v68, v72
	v_mul_f32_e32 v72, v72, v72
	v_fmac_f32_e32 v72, v68, v68
	v_add_f32_e32 v94, 0, v69
	v_lshlrev_b32_e32 v68, 16, v73
	v_and_b32_e32 v73, 0xffff0000, v73
	v_add_f32_e32 v69, v68, v73
	v_mul_f32_e32 v73, v73, v73
	v_fmac_f32_e32 v73, v68, v68
	v_add_f32_e32 v94, v69, v94
	v_add_f32_e32 v102, v72, v73
	v_lshlrev_b32_e32 v68, 16, v74
	v_and_b32_e32 v74, 0xffff0000, v74
	v_add_f32_e32 v69, v68, v74
	v_mul_f32_e32 v74, v74, v74
	v_fmac_f32_e32 v74, v68, v68
	v_add_f32_e32 v94, v69, v94
	v_add_f32_e32 v102, v74, v102
	v_lshlrev_b32_e32 v68, 16, v75
	v_and_b32_e32 v75, 0xffff0000, v75
	v_add_f32_e32 v69, v68, v75
	v_mul_f32_e32 v75, v75, v75
	v_fmac_f32_e32 v75, v68, v68
	v_add_f32_e32 v94, v69, v94
	v_add_f32_e32 v102, v75, v102
	v_lshlrev_b32_e32 v68, 16, v76
	v_and_b32_e32 v76, 0xffff0000, v76
	v_add_f32_e32 v69, v68, v76
	v_mul_f32_e32 v76, v76, v76
	v_fmac_f32_e32 v76, v68, v68
	v_add_f32_e32 v94, v69, v94
	v_add_f32_e32 v102, v76, v102
	v_lshlrev_b32_e32 v68, 16, v77
	v_and_b32_e32 v77, 0xffff0000, v77
	v_add_f32_e32 v69, v68, v77
	v_mul_f32_e32 v77, v77, v77
	v_fmac_f32_e32 v77, v68, v68
	v_add_f32_e32 v94, v69, v94
	v_add_f32_e32 v102, v77, v102
	v_lshlrev_b32_e32 v68, 16, v78
	v_and_b32_e32 v78, 0xffff0000, v78
	v_add_f32_e32 v69, v68, v78
	v_mul_f32_e32 v78, v78, v78
	v_fmac_f32_e32 v78, v68, v68
	v_add_f32_e32 v94, v69, v94
	v_add_f32_e32 v102, v78, v102
	v_lshlrev_b32_e32 v68, 16, v79
	v_and_b32_e32 v79, 0xffff0000, v79
	v_add_f32_e32 v69, v68, v79
	v_mul_f32_e32 v79, v79, v79
	v_fmac_f32_e32 v79, v68, v68
	v_add_f32_e32 v94, v69, v94
	v_add_f32_e32 v102, v79, v102
	s_waitcnt vmcnt(0)
	v_lshlrev_b32_e32 v68, 16, v80
	v_and_b32_e32 v80, 0xffff0000, v80
	v_add_f32_e32 v69, v68, v80
	v_mul_f32_e32 v80, v80, v80
	v_fmac_f32_e32 v80, v68, v68
	v_add_f32_e32 v95, 0, v69
	v_lshlrev_b32_e32 v68, 16, v81
	v_and_b32_e32 v81, 0xffff0000, v81
	v_add_f32_e32 v69, v68, v81
	v_mul_f32_e32 v81, v81, v81
	v_fmac_f32_e32 v81, v68, v68
	v_add_f32_e32 v95, v69, v95
	v_add_f32_e32 v71, v80, v81
	v_lshlrev_b32_e32 v68, 16, v82
	v_and_b32_e32 v82, 0xffff0000, v82
	v_add_f32_e32 v69, v68, v82
	v_mul_f32_e32 v82, v82, v82
	v_fmac_f32_e32 v82, v68, v68
	v_add_f32_e32 v95, v69, v95
	v_add_f32_e32 v71, v82, v71
	v_lshlrev_b32_e32 v68, 16, v83
	v_and_b32_e32 v83, 0xffff0000, v83
	v_add_f32_e32 v69, v68, v83
	v_mul_f32_e32 v83, v83, v83
	v_fmac_f32_e32 v83, v68, v68
	v_add_f32_e32 v95, v69, v95
	v_add_f32_e32 v71, v83, v71
	v_lshlrev_b32_e32 v68, 16, v84
	v_and_b32_e32 v84, 0xffff0000, v84
	v_add_f32_e32 v69, v68, v84
	v_mul_f32_e32 v84, v84, v84
	v_fmac_f32_e32 v84, v68, v68
	v_add_f32_e32 v95, v69, v95
	v_add_f32_e32 v71, v84, v71
	v_lshlrev_b32_e32 v68, 16, v85
	v_and_b32_e32 v85, 0xffff0000, v85
	v_add_f32_e32 v69, v68, v85
	v_mul_f32_e32 v85, v85, v85
	v_fmac_f32_e32 v85, v68, v68
	v_add_f32_e32 v95, v69, v95
	v_add_f32_e32 v71, v85, v71
	v_lshlrev_b32_e32 v68, 16, v86
	v_and_b32_e32 v86, 0xffff0000, v86
	v_add_f32_e32 v69, v68, v86
	v_mul_f32_e32 v86, v86, v86
	v_fmac_f32_e32 v86, v68, v68
	v_add_f32_e32 v95, v69, v95
	v_add_f32_e32 v71, v86, v71
	v_lshlrev_b32_e32 v68, 16, v87
	v_and_b32_e32 v87, 0xffff0000, v87
	v_add_f32_e32 v69, v68, v87
	v_mul_f32_e32 v87, v87, v87
	v_fmac_f32_e32 v87, v68, v68
	v_add_f32_e32 v95, v69, v95
	v_add_f32_e32 v71, v87, v71
	ds_bpermute_b32 v20, v5, v88
	ds_bpermute_b32 v21, v5, v89
	ds_bpermute_b32 v22, v5, v90
	ds_bpermute_b32 v23, v5, v91
	ds_bpermute_b32 v24, v5, v92
	ds_bpermute_b32 v25, v5, v93
	ds_bpermute_b32 v26, v5, v94
	ds_bpermute_b32 v27, v5, v95
	s_waitcnt lgkmcnt(0)
	v_add_f32_e32 v88, v88, v20
	v_add_f32_e32 v89, v89, v21
	v_add_f32_e32 v90, v90, v22
	v_add_f32_e32 v91, v91, v23
	v_add_f32_e32 v92, v92, v24
	v_add_f32_e32 v93, v93, v25
	v_add_f32_e32 v94, v94, v26
	v_add_f32_e32 v95, v95, v27
	ds_bpermute_b32 v20, v5, v96
	ds_bpermute_b32 v21, v5, v97
	ds_bpermute_b32 v22, v5, v98
	ds_bpermute_b32 v23, v5, v99
	ds_bpermute_b32 v24, v5, v100
	ds_bpermute_b32 v25, v5, v101
	ds_bpermute_b32 v26, v5, v102
	ds_bpermute_b32 v27, v5, v71
	s_waitcnt lgkmcnt(0)
	v_add_f32_e32 v96, v96, v20
	v_add_f32_e32 v97, v97, v21
	v_add_f32_e32 v98, v98, v22
	v_add_f32_e32 v99, v99, v23
	v_add_f32_e32 v100, v100, v24
	v_add_f32_e32 v101, v101, v25
	v_add_f32_e32 v102, v102, v26
	v_add_f32_e32 v71, v71, v27
	ds_bpermute_b32 v20, v6, v88
	ds_bpermute_b32 v21, v6, v89
	ds_bpermute_b32 v22, v6, v90
	ds_bpermute_b32 v23, v6, v91
	ds_bpermute_b32 v24, v6, v92
	ds_bpermute_b32 v25, v6, v93
	ds_bpermute_b32 v26, v6, v94
	ds_bpermute_b32 v27, v6, v95
	s_waitcnt lgkmcnt(0)
	v_add_f32_e32 v88, v88, v20
	v_add_f32_e32 v89, v89, v21
	v_add_f32_e32 v90, v90, v22
	v_add_f32_e32 v91, v91, v23
	v_add_f32_e32 v92, v92, v24
	v_add_f32_e32 v93, v93, v25
	v_add_f32_e32 v94, v94, v26
	v_add_f32_e32 v95, v95, v27
	ds_bpermute_b32 v20, v6, v96
	ds_bpermute_b32 v21, v6, v97
	ds_bpermute_b32 v22, v6, v98
	ds_bpermute_b32 v23, v6, v99
	ds_bpermute_b32 v24, v6, v100
	ds_bpermute_b32 v25, v6, v101
	ds_bpermute_b32 v26, v6, v102
	ds_bpermute_b32 v27, v6, v71
	s_waitcnt lgkmcnt(0)
	v_add_f32_e32 v96, v96, v20
	v_add_f32_e32 v97, v97, v21
	v_add_f32_e32 v98, v98, v22
	v_add_f32_e32 v99, v99, v23
	v_add_f32_e32 v100, v100, v24
	v_add_f32_e32 v101, v101, v25
	v_add_f32_e32 v102, v102, v26
	v_add_f32_e32 v71, v71, v27
	ds_bpermute_b32 v20, v7, v88
	ds_bpermute_b32 v21, v7, v89
	ds_bpermute_b32 v22, v7, v90
	ds_bpermute_b32 v23, v7, v91
	ds_bpermute_b32 v24, v7, v92
	ds_bpermute_b32 v25, v7, v93
	ds_bpermute_b32 v26, v7, v94
	ds_bpermute_b32 v27, v7, v95
	s_waitcnt lgkmcnt(0)
; __device__ __forceinline__ void unit(LAS unsigned char* lds, const bf16* Z, const bf16* sgw, const float* lng, const float* lnb, const float* sgb, bf16* OBp, int b, int nchunk, int g0, int ng, const int tid_in) {
;     ...
;         s = wave_sum(s); ss = wave_sum(ss);
;         const float mean = s * (1.0f / 1024.0f); const float var = fmaxf(ss * (1.0f / 1024.0f) - mean * mean, 0.f);
;         if (lane == 0) { STAT[tok * 2] = mean; STAT[tok * 2 + 1] = 1.0f / sqrtf(var + EPS); } }
	v_add_f32_e32 v88, v88, v20
	v_add_f32_e32 v89, v89, v21
	v_add_f32_e32 v90, v90, v22
	v_add_f32_e32 v91, v91, v23
	v_add_f32_e32 v92, v92, v24
	v_add_f32_e32 v93, v93, v25
	v_add_f32_e32 v94, v94, v26
	v_add_f32_e32 v95, v95, v27
	ds_bpermute_b32 v20, v7, v96
	ds_bpermute_b32 v21, v7, v97
	ds_bpermute_b32 v22, v7, v98
	ds_bpermute_b32 v23, v7, v99
	ds_bpermute_b32 v24, v7, v100
	ds_bpermute_b32 v25, v7, v101
	ds_bpermute_b32 v26, v7, v102
	ds_bpermute_b32 v27, v7, v71
	s_waitcnt lgkmcnt(0)
	v_add_f32_e32 v96, v96, v20
	v_add_f32_e32 v97, v97, v21
	v_add_f32_e32 v98, v98, v22
	v_add_f32_e32 v99, v99, v23
	v_add_f32_e32 v100, v100, v24
	v_add_f32_e32 v101, v101, v25
	v_add_f32_e32 v102, v102, v26
	v_add_f32_e32 v71, v71, v27
	ds_bpermute_b32 v20, v8, v88
	ds_bpermute_b32 v21, v8, v89
	ds_bpermute_b32 v22, v8, v90
	ds_bpermute_b32 v23, v8, v91
	ds_bpermute_b32 v24, v8, v92
	ds_bpermute_b32 v25, v8, v93
	ds_bpermute_b32 v26, v8, v94
	ds_bpermute_b32 v27, v8, v95
	s_waitcnt lgkmcnt(0)
	v_add_f32_e32 v88, v88, v20
	v_add_f32_e32 v89, v89, v21
	v_add_f32_e32 v90, v90, v22
	v_add_f32_e32 v91, v91, v23
	v_add_f32_e32 v92, v92, v24
	v_add_f32_e32 v93, v93, v25
	v_add_f32_e32 v94, v94, v26
	v_add_f32_e32 v95, v95, v27
	ds_bpermute_b32 v20, v8, v96
	ds_bpermute_b32 v21, v8, v97
	ds_bpermute_b32 v22, v8, v98
	ds_bpermute_b32 v23, v8, v99
	ds_bpermute_b32 v24, v8, v100
	ds_bpermute_b32 v25, v8, v101
	ds_bpermute_b32 v26, v8, v102
	ds_bpermute_b32 v27, v8, v71
	s_waitcnt lgkmcnt(0)
	v_add_f32_e32 v96, v96, v20
	v_add_f32_e32 v97, v97, v21
	v_add_f32_e32 v98, v98, v22
	v_add_f32_e32 v99, v99, v23
	v_add_f32_e32 v100, v100, v24
	v_add_f32_e32 v101, v101, v25
	v_add_f32_e32 v102, v102, v26
	v_add_f32_e32 v71, v71, v27
	ds_bpermute_b32 v20, v9, v88
	ds_bpermute_b32 v21, v9, v89
	ds_bpermute_b32 v22, v9, v90
	ds_bpermute_b32 v23, v9, v91
	ds_bpermute_b32 v24, v9, v92
	ds_bpermute_b32 v25, v9, v93
	ds_bpermute_b32 v26, v9, v94
	ds_bpermute_b32 v27, v9, v95
	s_waitcnt lgkmcnt(0)
	v_add_f32_e32 v88, v88, v20
	v_add_f32_e32 v89, v89, v21
	v_add_f32_e32 v90, v90, v22
	v_add_f32_e32 v91, v91, v23
	v_add_f32_e32 v92, v92, v24
	v_add_f32_e32 v93, v93, v25
	v_add_f32_e32 v94, v94, v26
	v_add_f32_e32 v95, v95, v27
	ds_bpermute_b32 v20, v9, v96
	ds_bpermute_b32 v21, v9, v97
	ds_bpermute_b32 v22, v9, v98
	ds_bpermute_b32 v23, v9, v99
	ds_bpermute_b32 v24, v9, v100
	ds_bpermute_b32 v25, v9, v101
	ds_bpermute_b32 v26, v9, v102
	ds_bpermute_b32 v27, v9, v71
	s_waitcnt lgkmcnt(0)
	v_add_f32_e32 v96, v96, v20
	v_add_f32_e32 v97, v97, v21
	v_add_f32_e32 v98, v98, v22
	v_add_f32_e32 v99, v99, v23
	v_add_f32_e32 v100, v100, v24
	v_add_f32_e32 v101, v101, v25
	v_add_f32_e32 v102, v102, v26
	v_add_f32_e32 v71, v71, v27
	ds_bpermute_b32 v20, v10, v88
	ds_bpermute_b32 v21, v10, v89
	ds_bpermute_b32 v22, v10, v90
	ds_bpermute_b32 v23, v10, v91
	ds_bpermute_b32 v24, v10, v92
	ds_bpermute_b32 v25, v10, v93
	ds_bpermute_b32 v26, v10, v94
	ds_bpermute_b32 v27, v10, v95
	s_waitcnt lgkmcnt(0)
	v_add_f32_e32 v88, v88, v20
	v_add_f32_e32 v89, v89, v21
	v_add_f32_e32 v90, v90, v22
	v_add_f32_e32 v91, v91, v23
	v_add_f32_e32 v92, v92, v24
	v_add_f32_e32 v93, v93, v25
	v_add_f32_e32 v94, v94, v26
	v_add_f32_e32 v95, v95, v27
	ds_bpermute_b32 v20, v10, v96
	ds_bpermute_b32 v21, v10, v97
	ds_bpermute_b32 v22, v10, v98
	ds_bpermute_b32 v23, v10, v99
	ds_bpermute_b32 v24, v10, v100
	ds_bpermute_b32 v25, v10, v101
	ds_bpermute_b32 v26, v10, v102
	ds_bpermute_b32 v27, v10, v71
	s_waitcnt lgkmcnt(0)
	v_add_f32_e32 v96, v96, v20
	v_add_f32_e32 v97, v97, v21
	v_add_f32_e32 v98, v98, v22
	v_add_f32_e32 v99, v99, v23
	v_add_f32_e32 v100, v100, v24
	v_add_f32_e32 v101, v101, v25
	v_add_f32_e32 v102, v102, v26
	v_add_f32_e32 v71, v71, v27
	s_and_saveexec_b64 s[16:17], s[0:1]
	s_cbranch_execz .Lsgu_ln_skip1
	v_mul_f32_e32 v12, 0x3a800000, v88
	v_mul_f32_e32 v11, v12, v12
	s_mov_b32 s4, 0x3a800000
	v_fma_f32 v11, v96, s4, -v11
	v_max_f32_e32 v11, 0, v11
	v_add_f32_e32 v11, 0x3727c5ac, v11
	s_mov_b32 s4, 0xf800000
	v_mul_f32_e32 v13, 0x4f800000, v11
	v_cmp_gt_f32_e32 vcc, s4, v11
	s_nop 1
	v_cndmask_b32_e32 v11, v11, v13, vcc
	v_sqrt_f32_e32 v13, v11
	s_nop 0
	v_add_u32_e32 v14, -1, v13
	v_fma_f32 v15, -v14, v13, v11
	v_cmp_ge_f32_e64 s[4:5], 0, v15
	v_add_u32_e32 v15, 1, v13
	s_nop 0
	v_cndmask_b32_e64 v14, v13, v14, s[4:5]
	v_fma_f32 v13, -v15, v13, v11
	v_cmp_lt_f32_e64 s[4:5], 0, v13
	s_nop 1
	v_cndmask_b32_e64 v13, v14, v15, s[4:5]
	v_mul_f32_e32 v14, 0x37800000, v13
	v_cndmask_b32_e32 v13, v13, v14, vcc
	v_cmp_class_f32_e32 vcc, v11, v225
	s_nop 1
	v_cndmask_b32_e32 v11, v13, v11, vcc
	v_div_scale_f32 v13, s[4:5], v11, v11, 1.0
	v_rcp_f32_e32 v14, v13
	s_add_i32 s4, s28, 0x19840
	v_fma_f32 v15, -v13, v14, 1.0
	v_fmac_f32_e32 v14, v15, v14
	v_div_scale_f32 v15, vcc, 1.0, v11, 1.0
	v_mul_f32_e32 v16, v15, v14
	v_fma_f32 v17, -v13, v16, v15
	v_fmac_f32_e32 v16, v17, v14
	v_fma_f32 v13, -v13, v16, v15
	s_nop 1
	v_div_fmas_f32 v13, v13, v14, v16
	v_div_fixup_f32 v13, v13, v11, 1.0
	v_mov_b32_e32 v11, s4
	ds_write_b64 v11, v[12:13]
	v_mul_f32_e32 v12, 0x3a800000, v89
	v_mul_f32_e32 v11, v12, v12
	s_mov_b32 s4, 0x3a800000
	v_fma_f32 v11, v97, s4, -v11
	v_max_f32_e32 v11, 0, v11
	v_add_f32_e32 v11, 0x3727c5ac, v11
	s_mov_b32 s4, 0xf800000
	v_mul_f32_e32 v13, 0x4f800000, v11
	v_cmp_gt_f32_e32 vcc, s4, v11
	s_nop 1
	v_cndmask_b32_e32 v11, v11, v13, vcc
	v_sqrt_f32_e32 v13, v11
	s_nop 0
	v_add_u32_e32 v14, -1, v13
	v_fma_f32 v15, -v14, v13, v11
	v_cmp_ge_f32_e64 s[4:5], 0, v15
	v_add_u32_e32 v15, 1, v13
	s_nop 0
	v_cndmask_b32_e64 v14, v13, v14, s[4:5]
	v_fma_f32 v13, -v15, v13, v11
	v_cmp_lt_f32_e64 s[4:5], 0, v13
; __device__ __forceinline__ void unit(LAS unsigned char* lds, const bf16* Z, const bf16* sgw, const float* lng, const float* lnb, const float* sgb, bf16* OBp, int b, int nchunk, int g0, int ng, const int tid_in) {
;     ...
;         const float mean = s * (1.0f / 1024.0f); const float var = fmaxf(ss * (1.0f / 1024.0f) - mean * mean, 0.f);
;         if (lane == 0) { STAT[tok * 2] = mean; STAT[tok * 2 + 1] = 1.0f / sqrtf(var + EPS); } }
	s_nop 1
	v_cndmask_b32_e64 v13, v14, v15, s[4:5]
	v_mul_f32_e32 v14, 0x37800000, v13
	v_cndmask_b32_e32 v13, v13, v14, vcc
	v_cmp_class_f32_e32 vcc, v11, v225
	s_nop 1
	v_cndmask_b32_e32 v11, v13, v11, vcc
	v_div_scale_f32 v13, s[4:5], v11, v11, 1.0
	v_rcp_f32_e32 v14, v13
	s_add_i32 s4, s28, 0x19848
	v_fma_f32 v15, -v13, v14, 1.0
	v_fmac_f32_e32 v14, v15, v14
	v_div_scale_f32 v15, vcc, 1.0, v11, 1.0
	v_mul_f32_e32 v16, v15, v14
	v_fma_f32 v17, -v13, v16, v15
	v_fmac_f32_e32 v16, v17, v14
	v_fma_f32 v13, -v13, v16, v15
	s_nop 1
	v_div_fmas_f32 v13, v13, v14, v16
	v_div_fixup_f32 v13, v13, v11, 1.0
	v_mov_b32_e32 v11, s4
	ds_write_b64 v11, v[12:13]
	v_mul_f32_e32 v12, 0x3a800000, v90
	v_mul_f32_e32 v11, v12, v12
	s_mov_b32 s4, 0x3a800000
	v_fma_f32 v11, v98, s4, -v11
	v_max_f32_e32 v11, 0, v11
	v_add_f32_e32 v11, 0x3727c5ac, v11
	s_mov_b32 s4, 0xf800000
	v_mul_f32_e32 v13, 0x4f800000, v11
	v_cmp_gt_f32_e32 vcc, s4, v11
	s_nop 1
	v_cndmask_b32_e32 v11, v11, v13, vcc
	v_sqrt_f32_e32 v13, v11
	s_nop 0
	v_add_u32_e32 v14, -1, v13
	v_fma_f32 v15, -v14, v13, v11
	v_cmp_ge_f32_e64 s[4:5], 0, v15
	v_add_u32_e32 v15, 1, v13
	s_nop 0
	v_cndmask_b32_e64 v14, v13, v14, s[4:5]
	v_fma_f32 v13, -v15, v13, v11
	v_cmp_lt_f32_e64 s[4:5], 0, v13
	s_nop 1
	v_cndmask_b32_e64 v13, v14, v15, s[4:5]
	v_mul_f32_e32 v14, 0x37800000, v13
	v_cndmask_b32_e32 v13, v13, v14, vcc
	v_cmp_class_f32_e32 vcc, v11, v225
	s_nop 1
	v_cndmask_b32_e32 v11, v13, v11, vcc
	v_div_scale_f32 v13, s[4:5], v11, v11, 1.0
	v_rcp_f32_e32 v14, v13
	s_add_i32 s4, s28, 0x19850
	v_fma_f32 v15, -v13, v14, 1.0
	v_fmac_f32_e32 v14, v15, v14
	v_div_scale_f32 v15, vcc, 1.0, v11, 1.0
	v_mul_f32_e32 v16, v15, v14
	v_fma_f32 v17, -v13, v16, v15
	v_fmac_f32_e32 v16, v17, v14
	v_fma_f32 v13, -v13, v16, v15
	s_nop 1
	v_div_fmas_f32 v13, v13, v14, v16
	v_div_fixup_f32 v13, v13, v11, 1.0
	v_mov_b32_e32 v11, s4
	ds_write_b64 v11, v[12:13]
	v_mul_f32_e32 v12, 0x3a800000, v91
	v_mul_f32_e32 v11, v12, v12
	s_mov_b32 s4, 0x3a800000
	v_fma_f32 v11, v99, s4, -v11
	v_max_f32_e32 v11, 0, v11
	v_add_f32_e32 v11, 0x3727c5ac, v11
	s_mov_b32 s4, 0xf800000
	v_mul_f32_e32 v13, 0x4f800000, v11
	v_cmp_gt_f32_e32 vcc, s4, v11
	s_nop 1
	v_cndmask_b32_e32 v11, v11, v13, vcc
	v_sqrt_f32_e32 v13, v11
	s_nop 0
	v_add_u32_e32 v14, -1, v13
	v_fma_f32 v15, -v14, v13, v11
	v_cmp_ge_f32_e64 s[4:5], 0, v15
	v_add_u32_e32 v15, 1, v13
	s_nop 0
	v_cndmask_b32_e64 v14, v13, v14, s[4:5]
	v_fma_f32 v13, -v15, v13, v11
	v_cmp_lt_f32_e64 s[4:5], 0, v13
	s_nop 1
	v_cndmask_b32_e64 v13, v14, v15, s[4:5]
	v_mul_f32_e32 v14, 0x37800000, v13
	v_cndmask_b32_e32 v13, v13, v14, vcc
	v_cmp_class_f32_e32 vcc, v11, v225
	s_nop 1
	v_cndmask_b32_e32 v11, v13, v11, vcc
	v_div_scale_f32 v13, s[4:5], v11, v11, 1.0
	v_rcp_f32_e32 v14, v13
	s_add_i32 s4, s28, 0x19858
	v_fma_f32 v15, -v13, v14, 1.0
	v_fmac_f32_e32 v14, v15, v14
	v_div_scale_f32 v15, vcc, 1.0, v11, 1.0
	v_mul_f32_e32 v16, v15, v14
	v_fma_f32 v17, -v13, v16, v15
	v_fmac_f32_e32 v16, v17, v14
	v_fma_f32 v13, -v13, v16, v15
	s_nop 1
	v_div_fmas_f32 v13, v13, v14, v16
	v_div_fixup_f32 v13, v13, v11, 1.0
	v_mov_b32_e32 v11, s4
	ds_write_b64 v11, v[12:13]
	v_mul_f32_e32 v12, 0x3a800000, v92
	v_mul_f32_e32 v11, v12, v12
	s_mov_b32 s4, 0x3a800000
	v_fma_f32 v11, v100, s4, -v11
	v_max_f32_e32 v11, 0, v11
	v_add_f32_e32 v11, 0x3727c5ac, v11
	s_mov_b32 s4, 0xf800000
	v_mul_f32_e32 v13, 0x4f800000, v11
	v_cmp_gt_f32_e32 vcc, s4, v11
	s_nop 1
	v_cndmask_b32_e32 v11, v11, v13, vcc
	v_sqrt_f32_e32 v13, v11
	s_nop 0
	v_add_u32_e32 v14, -1, v13
	v_fma_f32 v15, -v14, v13, v11
	v_cmp_ge_f32_e64 s[4:5], 0, v15
	v_add_u32_e32 v15, 1, v13
	s_nop 0
	v_cndmask_b32_e64 v14, v13, v14, s[4:5]
	v_fma_f32 v13, -v15, v13, v11
	v_cmp_lt_f32_e64 s[4:5], 0, v13
	s_nop 1
	v_cndmask_b32_e64 v13, v14, v15, s[4:5]
	v_mul_f32_e32 v14, 0x37800000, v13
	v_cndmask_b32_e32 v13, v13, v14, vcc
	v_cmp_class_f32_e32 vcc, v11, v225
	s_nop 1
	v_cndmask_b32_e32 v11, v13, v11, vcc
	v_div_scale_f32 v13, s[4:5], v11, v11, 1.0
	v_rcp_f32_e32 v14, v13
	s_add_i32 s4, s28, 0x19860
	v_fma_f32 v15, -v13, v14, 1.0
	v_fmac_f32_e32 v14, v15, v14
	v_div_scale_f32 v15, vcc, 1.0, v11, 1.0
	v_mul_f32_e32 v16, v15, v14
	v_fma_f32 v17, -v13, v16, v15
	v_fmac_f32_e32 v16, v17, v14
	v_fma_f32 v13, -v13, v16, v15
	s_nop 1
	v_div_fmas_f32 v13, v13, v14, v16
	v_div_fixup_f32 v13, v13, v11, 1.0
	v_mov_b32_e32 v11, s4
	ds_write_b64 v11, v[12:13]
	v_mul_f32_e32 v12, 0x3a800000, v93
	v_mul_f32_e32 v11, v12, v12
	s_mov_b32 s4, 0x3a800000
	v_fma_f32 v11, v101, s4, -v11
	v_max_f32_e32 v11, 0, v11
	v_add_f32_e32 v11, 0x3727c5ac, v11
	s_mov_b32 s4, 0xf800000
	v_mul_f32_e32 v13, 0x4f800000, v11
	v_cmp_gt_f32_e32 vcc, s4, v11
	s_nop 1
	v_cndmask_b32_e32 v11, v11, v13, vcc
	v_sqrt_f32_e32 v13, v11
	s_nop 0
	v_add_u32_e32 v14, -1, v13
	v_fma_f32 v15, -v14, v13, v11
	v_cmp_ge_f32_e64 s[4:5], 0, v15
	v_add_u32_e32 v15, 1, v13
	s_nop 0
	v_cndmask_b32_e64 v14, v13, v14, s[4:5]
	v_fma_f32 v13, -v15, v13, v11
	v_cmp_lt_f32_e64 s[4:5], 0, v13
	s_nop 1
	v_cndmask_b32_e64 v13, v14, v15, s[4:5]
	v_mul_f32_e32 v14, 0x37800000, v13
	v_cndmask_b32_e32 v13, v13, v14, vcc
	v_cmp_class_f32_e32 vcc, v11, v225
	s_nop 1
	v_cndmask_b32_e32 v11, v13, v11, vcc
	v_div_scale_f32 v13, s[4:5], v11, v11, 1.0
	v_rcp_f32_e32 v14, v13
	s_add_i32 s4, s28, 0x19868
	v_fma_f32 v15, -v13, v14, 1.0
	v_fmac_f32_e32 v14, v15, v14
	v_div_scale_f32 v15, vcc, 1.0, v11, 1.0
	v_mul_f32_e32 v16, v15, v14
	v_fma_f32 v17, -v13, v16, v15
	v_fmac_f32_e32 v16, v17, v14
	v_fma_f32 v13, -v13, v16, v15
	s_nop 1
	v_div_fmas_f32 v13, v13, v14, v16
	v_div_fixup_f32 v13, v13, v11, 1.0
	v_mov_b32_e32 v11, s4
	ds_write_b64 v11, v[12:13]
; #define LAS __attribute__((address_space(3)))
; __device__ __forceinline__ unsigned f2bf(float f) { unsigned u = __builtin_bit_cast(unsigned, f); return (u + 0x7fffu + ((u >> 16) & 1u)) >> 16; }
; __device__ __forceinline__ void unit(LAS unsigned char* lds, const bf16* Z, const bf16* sgw, const float* lng, const float* lnb, const float* sgb, bf16* OBp, int b, int nchunk, int g0, int ng, const int tid_in) {
;     ...
;         const float mean = s * (1.0f / 1024.0f); const float var = fmaxf(ss * (1.0f / 1024.0f) - mean * mean, 0.f);
;         if (lane == 0) { STAT[tok * 2] = mean; STAT[tok * 2 + 1] = 1.0f / sqrtf(var + EPS); } }
;     ...
; #pragma unroll 1
;     for (int g = g0; g < g0 + ng; ++g) {
;         if (tid < 128) BL[tid] = sgb[g * 128 + tid];
; #pragma unroll
;         for (int q = 0; q < 4; ++q) { const int idx = tid + 512 * q, row = idx >> 4, ch = idx & 15;
;             *(LAS v4u*)(WL + row * ST + ch * 8) = *(const v4u*)(sgw + (size_t)(g * 128 + row) * 128 + ch * 8);
;             *(LAS v4u*)(UL + row * ST + ch * 8) = *(const v4u*)(Z + (size_t)(tb0 + row) * ZLD + ZU + g * 128 + ch * 8);
;             const v4u vv = *(const v4u*)(Z + (size_t)(tb0 + row) * ZLD + ZV + g * 128 + ch * 8); const unsigned ww[4] = {vv.x, vv.y, vv.z, vv.w};
;             const float mean = STAT[row * 2], rstd = STAT[row * 2 + 1];
; #pragma unroll
;             for (int e = 0; e < 4; ++e) { const int c0 = g * 128 + ch * 8 + 2 * e;
;                 const float a = (bflo(ww[e]) - mean) * rstd * lng[c0] + lnb[c0], c = (bfhi(ww[e]) - mean) * rstd * lng[c0 + 1] + lnb[c0 + 1];
;                 VL[(ch * 8 + 2 * e) * ST + row] = (bf16)f2bf(a); VL[(ch * 8 + 2 * e + 1) * ST + row] = (bf16)f2bf(c); } }
	v_mul_f32_e32 v12, 0x3a800000, v94
	v_mul_f32_e32 v11, v12, v12
	s_mov_b32 s4, 0x3a800000
	v_fma_f32 v11, v102, s4, -v11
	v_max_f32_e32 v11, 0, v11
	v_add_f32_e32 v11, 0x3727c5ac, v11
	s_mov_b32 s4, 0xf800000
	v_mul_f32_e32 v13, 0x4f800000, v11
	v_cmp_gt_f32_e32 vcc, s4, v11
	s_nop 1
	v_cndmask_b32_e32 v11, v11, v13, vcc
	v_sqrt_f32_e32 v13, v11
	s_nop 0
	v_add_u32_e32 v14, -1, v13
	v_fma_f32 v15, -v14, v13, v11
	v_cmp_ge_f32_e64 s[4:5], 0, v15
	v_add_u32_e32 v15, 1, v13
	s_nop 0
	v_cndmask_b32_e64 v14, v13, v14, s[4:5]
	v_fma_f32 v13, -v15, v13, v11
	v_cmp_lt_f32_e64 s[4:5], 0, v13
	s_nop 1
	v_cndmask_b32_e64 v13, v14, v15, s[4:5]
	v_mul_f32_e32 v14, 0x37800000, v13
	v_cndmask_b32_e32 v13, v13, v14, vcc
	v_cmp_class_f32_e32 vcc, v11, v225
	s_nop 1
	v_cndmask_b32_e32 v11, v13, v11, vcc
	v_div_scale_f32 v13, s[4:5], v11, v11, 1.0
	v_rcp_f32_e32 v14, v13
	s_add_i32 s4, s28, 0x19870
	v_fma_f32 v15, -v13, v14, 1.0
	v_fmac_f32_e32 v14, v15, v14
	v_div_scale_f32 v15, vcc, 1.0, v11, 1.0
	v_mul_f32_e32 v16, v15, v14
	v_fma_f32 v17, -v13, v16, v15
	v_fmac_f32_e32 v16, v17, v14
	v_fma_f32 v13, -v13, v16, v15
	s_nop 1
	v_div_fmas_f32 v13, v13, v14, v16
	v_div_fixup_f32 v13, v13, v11, 1.0
	v_mov_b32_e32 v11, s4
	ds_write_b64 v11, v[12:13]
	v_mul_f32_e32 v12, 0x3a800000, v95
	v_mul_f32_e32 v11, v12, v12
	s_mov_b32 s4, 0x3a800000
	v_fma_f32 v11, v71, s4, -v11
	v_max_f32_e32 v11, 0, v11
	v_add_f32_e32 v11, 0x3727c5ac, v11
	s_mov_b32 s4, 0xf800000
	v_mul_f32_e32 v13, 0x4f800000, v11
	v_cmp_gt_f32_e32 vcc, s4, v11
	s_nop 1
	v_cndmask_b32_e32 v11, v11, v13, vcc
	v_sqrt_f32_e32 v13, v11
	s_nop 0
	v_add_u32_e32 v14, -1, v13
	v_fma_f32 v15, -v14, v13, v11
	v_cmp_ge_f32_e64 s[4:5], 0, v15
	v_add_u32_e32 v15, 1, v13
	s_nop 0
	v_cndmask_b32_e64 v14, v13, v14, s[4:5]
	v_fma_f32 v13, -v15, v13, v11
	v_cmp_lt_f32_e64 s[4:5], 0, v13
	s_nop 1
	v_cndmask_b32_e64 v13, v14, v15, s[4:5]
	v_mul_f32_e32 v14, 0x37800000, v13
	v_cndmask_b32_e32 v13, v13, v14, vcc
	v_cmp_class_f32_e32 vcc, v11, v225
	s_nop 1
	v_cndmask_b32_e32 v11, v13, v11, vcc
	v_div_scale_f32 v13, s[4:5], v11, v11, 1.0
	v_rcp_f32_e32 v14, v13
	s_add_i32 s4, s28, 0x19878
	v_fma_f32 v15, -v13, v14, 1.0
	v_fmac_f32_e32 v14, v15, v14
	v_div_scale_f32 v15, vcc, 1.0, v11, 1.0
	v_mul_f32_e32 v16, v15, v14
	v_fma_f32 v17, -v13, v16, v15
	v_fmac_f32_e32 v16, v17, v14
	v_fma_f32 v13, -v13, v16, v15
	s_nop 1
	v_div_fmas_f32 v13, v13, v14, v16
	v_div_fixup_f32 v13, v13, v11, 1.0
	v_mov_b32_e32 v11, s4
	ds_write_b64 v11, v[12:13]
.Lsgu_ln_skip1:
	s_or_b64 exec, exec, s[16:17]
.LBB0_293:
	s_lshl_b32 s0, s20, 2
	s_lshl_b32 s1, s20, 6
	s_ashr_i32 s15, s23, 7
	s_lshl_b32 s4, s22, 1
	s_and_b32 s14, s1, 0xffffff80
	s_and_b32 s21, s0, 4
	v_lshlrev_b32_e32 v2, 3, v70
	s_and_b32 s22, s4, 2
	s_lshl_b32 s23, s15, 1
	v_and_b32_e32 v71, 0x78, v2
	s_cmp_gt_i32 s15, -1
	s_waitcnt lgkmcnt(1)
	v_and_b32_e32 v12, 31, v70
	v_lshrrev_b32_e32 v13, 5, v4
	v_lshlrev_b32_e32 v186, 1, v71
	v_readlane_b32 s17, v254, 44
	s_cselect_b64 s[4:5], -1, 0
	s_lshl_b32 s16, s15, 5
	v_add_u32_e32 v72, s17, v186
	v_lshl_or_b32 v15, v13, 2, s16
	v_lshl_add_u32 v16, v12, 1, s17
	v_readlane_b32 s16, v251, 47
	v_readlane_b32 s17, v251, 48
	v_ashrrev_i32_e32 v74, 4, v70
	v_add_u32_e32 v2, s14, v74
	v_lshl_add_u64 v[44:45], s[16:17], 0, v[186:187]
	v_readlane_b32 s16, v253, 32
	v_readlane_b32 s17, v253, 33
	s_mov_b64 s[38:39], 0x1600
	s_mov_b64 s[40:41], 0x1e00
	v_mov_b64_e32 v[4:5], s[16:17]
	v_mad_i64_i32 v[6:7], s[16:17], v2, s26, v[4:5]
	v_lshl_add_u64 v[6:7], v[6:7], 0, v[186:187]
	v_lshl_add_u64 v[46:47], v[6:7], 0, s[38:39]
	v_lshl_add_u64 v[48:49], v[6:7], 0, s[40:41]
	v_add_u32_e32 v6, 0x200, v70
	v_ashrrev_i32_e32 v79, 4, v6
	s_waitcnt lgkmcnt(0)
	v_add_u32_e32 v14, 0, v186
	s_movk_i32 s16, 0x10e
	v_add_u32_e32 v6, s14, v79
	v_mad_u32_u24 v17, v71, s16, v14
	v_mad_i64_i32 v[8:9], s[16:17], v6, s26, v[4:5]
	v_lshl_add_u64 v[8:9], v[8:9], 0, v[186:187]
	v_lshl_add_u64 v[50:51], v[8:9], 0, s[38:39]
	v_lshl_add_u64 v[52:53], v[8:9], 0, s[40:41]
	v_add_u32_e32 v8, 0x400, v70
	s_movk_i32 s31, 0x110
	v_ashrrev_i32_e32 v84, 4, v8
	v_mul_lo_u32 v10, v79, s31
	v_add_u32_e32 v8, s14, v84
	v_add_u32_e32 v80, v14, v10
	v_add_u32_e32 v81, v72, v10
	v_mad_i64_i32 v[10:11], s[16:17], v8, s26, v[4:5]
	v_lshl_add_u64 v[10:11], v[10:11], 0, v[186:187]
	v_lshl_add_u64 v[54:55], v[10:11], 0, s[38:39]
	v_lshl_add_u64 v[56:57], v[10:11], 0, s[40:41]
	v_add_u32_e32 v10, 0x600, v70
	v_ashrrev_i32_e32 v89, 4, v10
	v_add_u32_e32 v10, s14, v89
	v_mad_i64_i32 v[4:5], s[16:17], v10, s26, v[4:5]
	v_lshl_add_u64 v[4:5], v[4:5], 0, v[186:187]
	s_or_b32 s14, s22, 1
	v_ashrrev_i32_e32 v3, 31, v2
	v_lshl_add_u64 v[58:59], v[4:5], 0, s[38:39]
	v_lshl_add_u64 v[60:61], v[4:5], 0, s[40:41]
	v_lshl_or_b32 v4, s22, 5, v12
	v_lshl_or_b32 v5, s14, 5, v12
	v_mul_u32_u24_e32 v4, 0x110, v4
	v_mul_u32_u24_e32 v5, 0x110, v5
	v_lshlrev_b64 v[62:63], 11, v[2:3]
	v_lshl_add_u32 v2, s14, 6, v16
	v_lshlrev_b32_e32 v3, 4, v13
	v_readlane_b32 s14, v254, 46
	v_mul_lo_u32 v18, v84, s31
	v_readlane_b32 s28, v254, 45
	v_add3_u32 v98, v5, v3, s14
	v_add3_u32 v99, v4, v3, s14
	s_mul_i32 s14, s15, 0x2200
	v_mul_lo_u32 v75, v74, s31
	v_add_u32_e32 v85, v14, v18
	v_add_u32_e32 v86, v72, v18
	v_mul_lo_u32 v18, v89, s31
	v_mov_b32_e32 v4, s14
	s_movk_i32 s0, 0x80
	v_add_u32_e32 v76, v14, v75
	v_lshl_add_u32 v78, v74, 1, v17
	v_ashrrev_i32_e32 v7, 31, v6
	v_lshl_add_u32 v83, v79, 1, v17
	v_ashrrev_i32_e32 v9, 31, v8
	v_lshl_add_u32 v88, v84, 1, v17
	v_add_u32_e32 v90, v14, v18
	v_ashrrev_i32_e32 v11, 31, v10
	v_lshl_add_u32 v93, v89, 1, v17
	v_mul_lo_u32 v14, v15, s31
	v_lshl_add_u32 v17, s22, 6, v16
	v_lshl_add_u32 v94, v15, 2, s28
	v_mad_u32_u24 v4, v12, s31, v4
	v_cmp_gt_i32_e64 s[0:1], s0, v70
	v_lshl_add_u64 v[42:43], s[6:7], 0, v[186:187]
	v_lshl_add_u32 v73, v70, 2, s28
	v_lshlrev_b32_e32 v77, 3, v74
	v_lshlrev_b32_e32 v82, 3, v79
	v_lshlrev_b32_e32 v87, 3, v84
	v_add_u32_e32 v91, v72, v18
	v_lshlrev_b32_e32 v92, 3, v89
	v_add_u32_e32 v95, 32, v94
	v_add_u32_e32 v96, 64, v94
	v_add_u32_e32 v97, 0x60, v94
	v_lshlrev_b64 v[64:65], 11, v[6:7]
	v_lshlrev_b64 v[66:67], 11, v[8:9]
	v_lshlrev_b64 v[68:69], 11, v[10:11]
	s_or_b32 s22, s21, 3
	s_add_i32 s23, s23, 2
	v_add3_u32 v100, v4, v3, 0
	v_add_u32_e32 v101, v17, v14
	v_add_u32_e32 v102, v2, v14
	s_barrier
	s_branch .LBB0_296
